# topk: hipcc's 4-way divergent candidate stage and lazily interleaved final bitonic layers replaced by uniform hand code (bitonic16 x2, unmono, select-by-fq inputs, one add + mono + pack per sidx): -48
# speedup vs baseline: 1.0078x; 1.0033x over previous
; #define LAS __attribute__((address_space(3)))
; __device__ __forceinline__ int phase_tid() { int t = (int)threadIdx.x; asm volatile("" : "+v"(t)); return t; }
; __device__ __forceinline__ int phase_wid(int tid) { return __builtin_amdgcn_readfirstlane(tid >> 6); }
; __device__ __forceinline__ unsigned mono(float f) { const unsigned u = __float_as_uint(f); return (u & 0x80000000u) ? ~u : (u ^ 0x80000000u); }
; __device__ __forceinline__ void topk_phase(LAS unsigned char* lds, const bf16_t* qp, const bf16_t* keys, const float* SU, const float* SV, int* sel_e, float* sel_g, float* sel_su, int G, int b) {
;     const int tid = phase_tid(), lane = tid & 63, wid = phase_wid(tid), fr = lane & 15, fq = lane >> 4;
;     LAS unsigned* wl = (LAS unsigned*)(lds + wid * 4096 + fr * 256);
;     LAS bf16_t* KL = (LAS bf16_t*)(lds + 32768);
;     pg8::StaticOrder SO; SO.init(S_, D_, G, b);
;     u32x4 kpre[8];
;     const int krow = tid >> 1, khf = tid & 1;
;     for (int ui = 0; ; ++ui) {
;         pg8::Unit gu; if (!SO.next(ui >> 1, gu)) break;
;         const int tt = gu.pm * 2 + (ui & 1), h = gu.pn;
;         const int tok = tt * 128 + wid * 16 + fr;
;     ...
;         for (int sidx = 0; sidx < 13; ++sidx) {
;             unsigned keyk[4];
; #pragma unroll
;             for (int k = 0; k < 4; ++k) {
;                 const int c = 4 * sidx + k;
;                 if (c < 50) { const int ci = cand_i(c), cj = cand_j(c); keyk[k] = (mono(v1[ci] + v2[cj]) & ~255u) | (unsigned)(255 - (ci * 16 + cj)); }
;                 else keyk[k] = 0u;
;             }
;             ck[sidx] = fq == 0 ? keyk[0] : fq == 1 ? keyk[1] : fq == 2 ? keyk[2] : keyk[3];
;         }
.LBB0_633:
	s_add_u32 s46, s92, 0x13800000
	s_addc_u32 s47, s93, 0
	s_add_u32 s48, s92, 0x14000000
	s_addc_u32 s49, s93, 0
	v_mov_b32_e32 v6, v0
	s_waitcnt vmcnt(0)
	s_barrier
	s_add_u32 s54, s92, 0x1c800000
	s_addc_u32 s55, s93, 0
	v_readfirstlane_b32 s0, v6
	v_ashrrev_i32_e32 v2, 1, v6
	s_ashr_i32 s0, s0, 6
	v_ashrrev_i32_e32 v3, 31, v2
	s_lshl_b32 s1, s0, 12
	v_lshlrev_b64 v[4:5], 8, v[2:3]
	v_lshlrev_b32_e32 v3, 7, v6
	v_and_b32_e32 v7, 15, v6
	s_add_i32 s1, s1, 0
	v_lshl_add_u64 v[4:5], s[92:93], 0, v[4:5]
	v_and_b32_e32 v78, 0x80, v3
	v_mov_b32_e32 v79, 0
	v_lshl_add_u32 v83, v7, 8, s1
	v_lshl_or_b32 v85, s0, 4, v7
	v_lshl_add_u64 v[4:5], v[4:5], 0, v[78:79]
	s_mov_b64 s[0:1], 0x1100000
	v_bfe_u32 v1, v6, 4, 2
	v_lshl_add_u64 v[80:81], v[4:5], 0, s[0:1]
	s_movk_i32 s0, 0x110
	v_mul_lo_u32 v2, v2, s0
	v_lshl_add_u32 v87, v1, 4, 0
	v_add_u32_e32 v3, 0, v2
	v_lshlrev_b32_e32 v2, 3, v1
	v_add_u32_e32 v4, 0x8000, v87
	v_lshlrev_b32_e32 v82, 2, v1
	v_mul_u32_u24_e32 v89, 0x110, v7
	s_mov_b32 s52, 0
	v_cmp_eq_u32_e64 s[38:39], 2, v1
	v_cmp_eq_u32_e64 s[40:41], 0, v1
	v_cmp_ne_u32_e64 s[42:43], 0, v1
	v_xor_b32_e32 v98, 0x7f, v82
	v_xor_b32_e32 v99, 63, v82
	v_xor_b32_e32 v100, 0x7e, v82
	v_xor_b32_e32 v101, 62, v82
	v_xor_b32_e32 v102, 0x7d, v82
	v_xor_b32_e32 v103, 61, v82
	v_xor_b32_e32 v104, 0x7c, v82
	v_xor_b32_e32 v105, 60, v82
	v_xor_b32_e32 v106, 0x6f, v82
	v_xor_b32_e32 v107, 47, v82
	v_xor_b32_e32 v108, 0x6e, v82
	v_xor_b32_e32 v109, 46, v82
	v_xor_b32_e32 v110, 0x6d, v82
	v_xor_b32_e32 v111, 45, v82
	v_xor_b32_e32 v112, 0x6c, v82
	v_xor_b32_e32 v113, 44, v82
	v_xor_b32_e32 v114, 0x5f, v82
	v_xor_b32_e32 v115, 31, v82
	v_xor_b32_e32 v116, 0x5e, v82
	v_xor_b32_e32 v117, 30, v82
	v_xor_b32_e32 v118, 0x5d, v82
	v_xor_b32_e32 v119, 29, v82
	v_xor_b32_e32 v120, 0x5c, v82
	v_xor_b32_e32 v121, 28, v82
	v_xor_b32_e32 v122, 0x4f, v82
	v_xor_b32_e32 v123, 15, v82
	v_xor_b32_e32 v124, 0x4e, v82
	v_xor_b32_e32 v125, 14, v82
	v_xor_b32_e32 v126, 0x4d, v82
	v_xor_b32_e32 v127, 13, v82
	v_xor_b32_e32 v128, 0x4c, v82
	v_xor_b32_e32 v129, 12, v82
	v_or_b32_e32 v84, 1, v82
	v_or_b32_e32 v86, 2, v82
	v_or_b32_e32 v88, 3, v82
	v_add_u32_e32 v130, v3, v78
	v_lshlrev_b32_e32 v78, 1, v2
	s_movk_i32 s53, 0xff80
	s_mov_b32 s12, 0x7fffff80
	s_mov_b32 s13, 0x7fffff00
	s_mov_b32 s14, 0x7fffffff
	v_add_u32_e32 v131, v4, v89
	s_movk_i32 s60, 0xff00
	s_movk_i32 s61, 0x3fff
	v_mov_b64_e32 v[90:91], 0x200
	v_mov_b64_e32 v[92:93], 0x1ff
	v_bfrev_b32_e32 v132, 1
	v_mov_b32_e32 v133, 0xffffff00
	v_cmp_eq_u32_e64 s[16:17], 1, v1
	v_cmp_eq_u32_e64 s[18:19], 2, v1
	v_cmp_eq_u32_e64 s[20:21], 3, v1
	v_cmp_lt_u32_e64 s[22:23], 1, v1
	s_nop 3
	s_or_b64 s[24:25], s[16:17], s[20:21]
	v_mov_b32_e32 v203, 0xff
	v_mov_b32_e32 v255, 0xfe
	v_cndmask_b32_e64 v203, v203, v255, s[16:17]
	v_mov_b32_e32 v255, 0xfd
	v_cndmask_b32_e64 v203, v203, v255, s[18:19]
	v_mov_b32_e32 v255, 0xfc
	v_cndmask_b32_e64 v203, v203, v255, s[20:21]
	v_mov_b32_e32 v204, 0xfb
	v_mov_b32_e32 v255, 0xfa
	v_cndmask_b32_e64 v204, v204, v255, s[16:17]
	v_mov_b32_e32 v255, 0xf9
	v_cndmask_b32_e64 v204, v204, v255, s[18:19]
	v_mov_b32_e32 v255, 0xf8
	v_cndmask_b32_e64 v204, v204, v255, s[20:21]
	v_mov_b32_e32 v205, 0xf7
	v_mov_b32_e32 v255, 0xf6
	v_cndmask_b32_e64 v205, v205, v255, s[16:17]
	v_mov_b32_e32 v255, 0xf5
	v_cndmask_b32_e64 v205, v205, v255, s[18:19]
	v_mov_b32_e32 v255, 0xf4
	v_cndmask_b32_e64 v205, v205, v255, s[20:21]
	v_mov_b32_e32 v206, 0xf3
	v_mov_b32_e32 v255, 0xf2
	v_cndmask_b32_e64 v206, v206, v255, s[16:17]
	v_mov_b32_e32 v255, 0xf1
	v_cndmask_b32_e64 v206, v206, v255, s[18:19]
	v_mov_b32_e32 v255, 0xf0
	v_cndmask_b32_e64 v206, v206, v255, s[20:21]
	v_mov_b32_e32 v207, 0xef
	v_mov_b32_e32 v255, 0xee
	v_cndmask_b32_e64 v207, v207, v255, s[16:17]
	v_mov_b32_e32 v255, 0xed
	v_cndmask_b32_e64 v207, v207, v255, s[18:19]
	v_mov_b32_e32 v255, 0xec
	v_cndmask_b32_e64 v207, v207, v255, s[20:21]
	v_mov_b32_e32 v208, 0xeb
	v_mov_b32_e32 v255, 0xea
	v_cndmask_b32_e64 v208, v208, v255, s[16:17]
	v_mov_b32_e32 v255, 0xe9
	v_cndmask_b32_e64 v208, v208, v255, s[18:19]
	v_mov_b32_e32 v255, 0xe8
	v_cndmask_b32_e64 v208, v208, v255, s[20:21]
	v_mov_b32_e32 v209, 0xdf
	v_mov_b32_e32 v255, 0xde
	v_cndmask_b32_e64 v209, v209, v255, s[16:17]
	v_mov_b32_e32 v255, 0xdd
	v_cndmask_b32_e64 v209, v209, v255, s[18:19]
	v_mov_b32_e32 v255, 0xdc
	v_cndmask_b32_e64 v209, v209, v255, s[20:21]
	v_mov_b32_e32 v210, 0xdb
	v_mov_b32_e32 v255, 0xcf
	v_cndmask_b32_e64 v210, v210, v255, s[16:17]
	v_mov_b32_e32 v255, 0xce
	v_cndmask_b32_e64 v210, v210, v255, s[18:19]
	v_mov_b32_e32 v255, 0xcd
	v_cndmask_b32_e64 v210, v210, v255, s[20:21]
	v_mov_b32_e32 v211, 0xcc
	v_mov_b32_e32 v255, 0xbf
	v_cndmask_b32_e64 v211, v211, v255, s[16:17]
	v_mov_b32_e32 v255, 0xbe
	v_cndmask_b32_e64 v211, v211, v255, s[18:19]
	v_mov_b32_e32 v255, 0xbd
	v_cndmask_b32_e64 v211, v211, v255, s[20:21]
	v_mov_b32_e32 v212, 0xaf
	v_mov_b32_e32 v255, 0xae
	v_cndmask_b32_e64 v212, v212, v255, s[16:17]
	v_mov_b32_e32 v255, 0x9f
	v_cndmask_b32_e64 v212, v212, v255, s[18:19]
	v_mov_b32_e32 v255, 0x9e
	v_cndmask_b32_e64 v212, v212, v255, s[20:21]
	v_mov_b32_e32 v213, 0x8f
	v_mov_b32_e32 v255, 0x8e
	v_cndmask_b32_e64 v213, v213, v255, s[16:17]
	v_mov_b32_e32 v255, 0x7f
	v_cndmask_b32_e64 v213, v213, v255, s[18:19]
	v_mov_b32_e32 v255, 0x6f
	v_cndmask_b32_e64 v213, v213, v255, s[20:21]
	v_mov_b32_e32 v214, 0x5f
	v_mov_b32_e32 v255, 0x4f
	v_cndmask_b32_e64 v214, v214, v255, s[16:17]
	v_mov_b32_e32 v255, 0x3f
	v_cndmask_b32_e64 v214, v214, v255, s[18:19]
	v_mov_b32_e32 v255, 0x2f
	v_cndmask_b32_e64 v214, v214, v255, s[20:21]
	v_mov_b32_e32 v215, 0x1f
	v_mov_b32_e32 v255, 0xf
	v_cndmask_b32_e64 v215, v215, v255, s[16:17]
	v_mov_b32_e32 v255, 0x0
	v_cndmask_b32_e64 v215, v215, v255, s[18:19]
	v_mov_b32_e32 v255, 0x0
	v_cndmask_b32_e64 v215, v215, v255, s[20:21]
	s_branch .LBB0_637

; #define LAS __attribute__((address_space(3)))
; __device__ __forceinline__ f32x4 mfma16(bf16x8 a, bf16x8 b, f32x4 c) { return __builtin_amdgcn_mfma_f32_16x16x32_bf16(a, b, c, 0, 0, 0); }
; __device__ __forceinline__ void topk_phase(LAS unsigned char* lds, const bf16_t* qp, const bf16_t* keys, const float* SU, const float* SV, int* sel_e, float* sel_g, float* sel_su, int G, int b) {
;     ...
;         for (int p = 0; p < 2; ++p) {
;             f32x4 acc[8];
; #pragma unroll
;             for (int mt = 0; mt < 8; ++mt) acc[mt] = (f32x4){0.f, 0.f, 0.f, 0.f};
;             bf16x8 bq[4];
; #pragma unroll
;             for (int ks = 0; ks < 4; ++ks) bq[ks] = *(const bf16x8*)(qp + (size_t)tok * D_ + h * 256 + p * 128 + ks * 32 + fq * 8);
;             const LAS bf16_t* kb = KL + p * 128 * 136;
; #pragma unroll
;             for (int mt = 0; mt < 8; ++mt)
; #pragma unroll
;                 for (int ks = 0; ks < 4; ++ks) { const bf16x8 a = *(const LAS bf16x8*)(kb + (mt * 16 + fr) * 136 + ks * 32 + fq * 8); acc[mt] = mfma16(a, bq[ks], acc[mt]); }
.LBB0_659:
	s_and_b32 s0, s52, 1
	s_lshl_b32 s1, s64, 8
	s_lshl_b32 s0, s0, 7
	s_or_b32 s0, s1, s0
	v_add_u32_e32 v94, s0, v85
	v_ashrrev_i32_e32 v95, 31, v94
	v_lshlrev_b64 v[34:35], 12, v[94:95]
	s_lshl_b32 s0, s56, 8
	v_lshl_add_u64 v[34:35], s[74:75], 0, v[34:35]
	s_ashr_i32 s1, s0, 31
	v_lshl_add_u64 v[34:35], s[0:1], 1, v[34:35]
	v_lshl_add_u64 v[96:97], v[34:35], 0, v[78:79]
	global_load_dwordx4 v[66:69], v[96:97], off
	global_load_dwordx4 v[62:65], v[96:97], off offset:64
	global_load_dwordx4 v[58:61], v[96:97], off offset:128
	global_load_dwordx4 v[54:57], v[96:97], off offset:192
	v_add_u32_e32 v138, v87, v89
	ds_read_b128 v[34:37], v138 offset:32768
	ds_read_b128 v[38:41], v138 offset:32832
	s_movk_i32 s0, 0xff
	s_waitcnt vmcnt(3) lgkmcnt(1)
	v_mfma_f32_16x16x32_bf16 v[34:37], v[34:37], v[66:69], 0
	ds_read_b128 v[42:45], v138 offset:41536
	ds_read_b128 v[50:53], v138 offset:45888
	ds_read_b128 v[70:73], v138 offset:50240
	s_waitcnt vmcnt(2) lgkmcnt(3)
	v_mfma_f32_16x16x32_bf16 v[34:37], v[38:41], v[62:65], v[34:37]
	ds_read_b128 v[38:41], v138 offset:32896
	ds_read_b128 v[74:77], v138 offset:54592
	ds_read_b128 v[134:137], v138 offset:58944
	s_waitcnt vmcnt(1) lgkmcnt(2)
	v_mfma_f32_16x16x32_bf16 v[34:37], v[38:41], v[58:61], v[34:37]
	ds_read_b128 v[38:41], v138 offset:32960
	s_waitcnt vmcnt(0) lgkmcnt(0)
	v_mfma_f32_16x16x32_bf16 v[46:49], v[38:41], v[54:57], v[34:37]
	s_nop 4
	ds_read_b128 v[34:37], v138 offset:37120
	ds_read_b128 v[38:41], v138 offset:37184
	s_nop 0
	s_waitcnt lgkmcnt(1)
	v_mfma_f32_16x16x32_bf16 v[34:37], v[34:37], v[66:69], 0
	s_waitcnt lgkmcnt(0)
	v_mfma_f32_16x16x32_bf16 v[34:37], v[38:41], v[62:65], v[34:37]
	ds_read_b128 v[38:41], v138 offset:37248
	s_waitcnt lgkmcnt(0)
	v_mfma_f32_16x16x32_bf16 v[34:37], v[38:41], v[58:61], v[34:37]
	ds_read_b128 v[38:41], v138 offset:37312
	s_waitcnt lgkmcnt(0)
	v_mfma_f32_16x16x32_bf16 v[34:37], v[38:41], v[54:57], v[34:37]
	ds_read_b128 v[38:41], v138 offset:41472
	s_waitcnt lgkmcnt(0)
	v_mfma_f32_16x16x32_bf16 v[38:41], v[38:41], v[66:69], 0
	v_mfma_f32_16x16x32_bf16 v[38:41], v[42:45], v[62:65], v[38:41]
	ds_read_b128 v[42:45], v138 offset:41600
	s_waitcnt lgkmcnt(0)
	v_mfma_f32_16x16x32_bf16 v[38:41], v[42:45], v[58:61], v[38:41]
	ds_read_b128 v[42:45], v138 offset:41664
	s_waitcnt lgkmcnt(0)
	v_mfma_f32_16x16x32_bf16 v[38:41], v[42:45], v[54:57], v[38:41]
	ds_read_b128 v[42:45], v138 offset:45824
	s_waitcnt lgkmcnt(0)
	v_mfma_f32_16x16x32_bf16 v[42:45], v[42:45], v[66:69], 0
	v_mfma_f32_16x16x32_bf16 v[42:45], v[50:53], v[62:65], v[42:45]
	ds_read_b128 v[50:53], v138 offset:45952
	s_waitcnt lgkmcnt(0)
	v_mfma_f32_16x16x32_bf16 v[42:45], v[50:53], v[58:61], v[42:45]
	ds_read_b128 v[50:53], v138 offset:46016
	s_waitcnt lgkmcnt(0)
	v_mfma_f32_16x16x32_bf16 v[42:45], v[50:53], v[54:57], v[42:45]
	ds_read_b128 v[50:53], v138 offset:50176
	s_waitcnt lgkmcnt(0)
	v_mfma_f32_16x16x32_bf16 v[50:53], v[50:53], v[66:69], 0
	v_mfma_f32_16x16x32_bf16 v[50:53], v[70:73], v[62:65], v[50:53]
	ds_read_b128 v[70:73], v138 offset:50304
	s_waitcnt lgkmcnt(0)
	v_mfma_f32_16x16x32_bf16 v[50:53], v[70:73], v[58:61], v[50:53]
	ds_read_b128 v[70:73], v138 offset:50368
	s_waitcnt lgkmcnt(0)
	v_mfma_f32_16x16x32_bf16 v[70:73], v[70:73], v[54:57], v[50:53]
	s_nop 4
	ds_read_b128 v[50:53], v138 offset:54528
	s_waitcnt lgkmcnt(0)
	v_mfma_f32_16x16x32_bf16 v[50:53], v[50:53], v[66:69], 0
	v_mfma_f32_16x16x32_bf16 v[50:53], v[74:77], v[62:65], v[50:53]
	ds_read_b128 v[74:77], v138 offset:54656
	s_waitcnt lgkmcnt(0)
	v_mfma_f32_16x16x32_bf16 v[50:53], v[74:77], v[58:61], v[50:53]
	ds_read_b128 v[74:77], v138 offset:54720
	s_waitcnt lgkmcnt(0)
	v_mfma_f32_16x16x32_bf16 v[50:53], v[74:77], v[54:57], v[50:53]
	ds_read_b128 v[74:77], v138 offset:58880
	s_waitcnt lgkmcnt(0)
	v_mfma_f32_16x16x32_bf16 v[74:77], v[74:77], v[66:69], 0
	v_mfma_f32_16x16x32_bf16 v[74:77], v[134:137], v[62:65], v[74:77]
	ds_read_b128 v[134:137], v138 offset:59008
	s_waitcnt lgkmcnt(0)
	v_mfma_f32_16x16x32_bf16 v[74:77], v[134:137], v[58:61], v[74:77]
	ds_read_b128 v[134:137], v138 offset:59072
	s_waitcnt lgkmcnt(0)
	v_mfma_f32_16x16x32_bf16 v[74:77], v[134:137], v[54:57], v[74:77]
	ds_read_b128 v[134:137], v138 offset:63232
	s_waitcnt lgkmcnt(0)
	v_mfma_f32_16x16x32_bf16 v[66:69], v[134:137], v[66:69], 0
	ds_read_b128 v[134:137], v138 offset:63296
	s_waitcnt lgkmcnt(0)
	v_mfma_f32_16x16x32_bf16 v[62:65], v[134:137], v[62:65], v[66:69]
	s_nop 4
	ds_read_b128 v[66:69], v138 offset:63360
	s_waitcnt lgkmcnt(0)
	v_mfma_f32_16x16x32_bf16 v[58:61], v[66:69], v[58:61], v[62:65]
	s_nop 2
	ds_read_b128 v[62:65], v138 offset:63424
	s_waitcnt lgkmcnt(0)
; #define LAS __attribute__((address_space(3)))
; __device__ __forceinline__ f32x4 mfma16(bf16x8 a, bf16x8 b, f32x4 c) { return __builtin_amdgcn_mfma_f32_16x16x32_bf16(a, b, c, 0, 0, 0); }
; __device__ __forceinline__ unsigned mono(float f) { const unsigned u = __float_as_uint(f); return (u & 0x80000000u) ? ~u : (u ^ 0x80000000u); }
; __device__ __forceinline__ void topk_phase(LAS unsigned char* lds, const bf16_t* qp, const bf16_t* keys, const float* SU, const float* SV, int* sel_e, float* sel_g, float* sel_su, int G, int b) {
;     ...
;                 for (int ks = 0; ks < 4; ++ks) { const bf16x8 a = *(const LAS bf16x8*)(kb + (mt * 16 + fr) * 136 + ks * 32 + fq * 8); acc[mt] = mfma16(a, bq[ks], acc[mt]); }
;             unsigned lo16[16];
; #pragma unroll
;             for (int mt = 0; mt < 4; ++mt)
; #pragma unroll
;                 for (int r = 0; r < 4; ++r) {
;                     T[p][mt * 4 + r] = (mono(acc[mt][r]) & ~127u) | (unsigned)(127 - (mt * 16 + fq * 4 + r));
;                     lo16[mt * 4 + r] = (mono(acc[mt + 4][r]) & ~127u) | (unsigned)(127 - ((mt + 4) * 16 + fq * 4 + r));
;                 }
;             SN_SORT16(T[p]); SN_SORT16(lo16);
	v_mfma_f32_16x16x32_bf16 v[54:57], v[62:65], v[54:57], v[58:61]
	s_nop 2
	v_ashrrev_i32_e32 v58, 31, v46
	v_bitop3_b32 v46, v46, v58, v132 bitop3:0x1e
	v_and_or_b32 v46, v46, s53, v98
	v_ashrrev_i32_e32 v58, 31, v70
	v_bitop3_b32 v58, v70, v58, v132 bitop3:0x1e
	v_and_or_b32 v58, v58, s53, v99
	v_ashrrev_i32_e32 v59, 31, v47
	v_bitop3_b32 v47, v47, v59, v132 bitop3:0x1e
	v_and_or_b32 v47, v47, s53, v100
	v_ashrrev_i32_e32 v59, 31, v71
	v_bitop3_b32 v59, v71, v59, v132 bitop3:0x1e
	v_and_or_b32 v59, v59, s53, v101
	v_ashrrev_i32_e32 v60, 31, v48
	v_bitop3_b32 v48, v48, v60, v132 bitop3:0x1e
	v_and_or_b32 v48, v48, s53, v102
	v_ashrrev_i32_e32 v60, 31, v72
	v_bitop3_b32 v60, v72, v60, v132 bitop3:0x1e
	v_and_or_b32 v60, v60, s53, v103
	v_ashrrev_i32_e32 v61, 31, v49
	v_bitop3_b32 v49, v49, v61, v132 bitop3:0x1e
	v_and_or_b32 v49, v49, s53, v104
	v_ashrrev_i32_e32 v61, 31, v73
	v_bitop3_b32 v61, v73, v61, v132 bitop3:0x1e
	v_and_or_b32 v61, v61, s53, v105
	v_ashrrev_i32_e32 v62, 31, v34
	v_bitop3_b32 v34, v34, v62, v132 bitop3:0x1e
	v_and_or_b32 v34, v34, s53, v106
	v_ashrrev_i32_e32 v62, 31, v50
	v_bitop3_b32 v50, v50, v62, v132 bitop3:0x1e
	v_and_or_b32 v50, v50, s53, v107
	v_ashrrev_i32_e32 v62, 31, v35
	v_bitop3_b32 v35, v35, v62, v132 bitop3:0x1e
	v_and_or_b32 v35, v35, s53, v108
	v_ashrrev_i32_e32 v62, 31, v51
	v_bitop3_b32 v51, v51, v62, v132 bitop3:0x1e
	v_and_or_b32 v51, v51, s53, v109
	v_ashrrev_i32_e32 v62, 31, v36
	v_bitop3_b32 v36, v36, v62, v132 bitop3:0x1e
	v_and_or_b32 v36, v36, s53, v110
	v_ashrrev_i32_e32 v62, 31, v52
	v_bitop3_b32 v52, v52, v62, v132 bitop3:0x1e
	v_and_or_b32 v52, v52, s53, v111
	v_ashrrev_i32_e32 v62, 31, v37
	v_bitop3_b32 v37, v37, v62, v132 bitop3:0x1e
	v_and_or_b32 v37, v37, s53, v112
	v_ashrrev_i32_e32 v62, 31, v53
	v_bitop3_b32 v53, v53, v62, v132 bitop3:0x1e
	v_and_or_b32 v53, v53, s53, v113
	v_ashrrev_i32_e32 v62, 31, v38
	v_bitop3_b32 v38, v38, v62, v132 bitop3:0x1e
	v_and_or_b32 v38, v38, s53, v114
	v_ashrrev_i32_e32 v62, 31, v74
	v_bitop3_b32 v62, v74, v62, v132 bitop3:0x1e
	v_max_u32_e32 v74, v58, v59
	v_ashrrev_i32_e32 v63, 31, v39
	v_cmp_lt_i32_e32 vcc, -1, v75
	v_bitop3_b32 v39, v39, v63, v132 bitop3:0x1e
	v_min_u32_e32 v58, v58, v59
	v_cndmask_b32_e32 v63, -1, v132, vcc
	v_max_u32_e32 v59, v60, v61
	v_min_u32_e32 v60, v60, v61
	v_ashrrev_i32_e32 v64, 31, v40
	v_cmp_lt_i32_e32 vcc, -1, v76
	v_bitop3_b32 v40, v40, v64, v132 bitop3:0x1e
	v_max_u32_e32 v61, v74, v59
	v_cndmask_b32_e32 v64, -1, v132, vcc
	v_min_u32_e32 v59, v74, v59
	v_max_u32_e32 v74, v58, v60
	v_ashrrev_i32_e32 v65, 31, v41
	v_cmp_lt_i32_e32 vcc, -1, v77
	v_bitop3_b32 v41, v41, v65, v132 bitop3:0x1e
	v_min_u32_e32 v58, v58, v60
	v_cndmask_b32_e32 v65, -1, v132, vcc
	v_max_u32_e32 v60, v74, v59
	v_min_u32_e32 v59, v74, v59
	v_ashrrev_i32_e32 v66, 31, v42
	v_bitop3_b32 v42, v42, v66, v132 bitop3:0x1e
	v_max_u32_e32 v74, v50, v51
	v_ashrrev_i32_e32 v66, 31, v54
	v_bitop3_b32 v54, v54, v66, v132 bitop3:0x1e
	v_min_u32_e32 v50, v50, v51
	v_ashrrev_i32_e32 v66, 31, v43
	v_bitop3_b32 v43, v43, v66, v132 bitop3:0x1e
	v_max_u32_e32 v51, v52, v53
	v_ashrrev_i32_e32 v66, 31, v55
	v_bitop3_b32 v55, v55, v66, v132 bitop3:0x1e
	v_min_u32_e32 v52, v52, v53
	v_ashrrev_i32_e32 v66, 31, v44
	v_bitop3_b32 v44, v44, v66, v132 bitop3:0x1e
	v_max_u32_e32 v53, v74, v51
	v_ashrrev_i32_e32 v66, 31, v56
	v_bitop3_b32 v56, v56, v66, v132 bitop3:0x1e
	v_min_u32_e32 v51, v74, v51
	v_ashrrev_i32_e32 v66, 31, v45
	v_cmp_lt_i32_e32 vcc, -1, v57
	v_bitop3_b32 v45, v45, v66, v132 bitop3:0x1e
	v_max_u32_e32 v74, v50, v52
	v_cndmask_b32_e32 v66, -1, v132, vcc
	v_xor_b32_e32 v57, v66, v57
	v_max_u32_e32 v66, v46, v47
	v_min_u32_e32 v46, v46, v47
	v_max_u32_e32 v47, v48, v49
	v_min_u32_e32 v48, v48, v49
	v_max_u32_e32 v49, v66, v47
	v_min_u32_e32 v47, v66, v47
	v_max_u32_e32 v66, v46, v48
	v_min_u32_e32 v46, v46, v48
	v_max_u32_e32 v48, v66, v47
	v_min_u32_e32 v47, v66, v47
	v_max_u32_e32 v66, v34, v35
	v_min_u32_e32 v34, v34, v35
	v_max_u32_e32 v35, v36, v37
	v_min_u32_e32 v36, v36, v37
	v_max_u32_e32 v37, v66, v35
	v_min_u32_e32 v35, v66, v35
	v_max_u32_e32 v66, v34, v36
	v_min_u32_e32 v34, v34, v36
	v_max_u32_e32 v36, v66, v35
	v_min_u32_e32 v35, v66, v35
	v_min_u32_e32 v50, v50, v52
	v_max_u32_e32 v52, v74, v51
	v_min_u32_e32 v51, v74, v51
	v_max_u32_e32 v66, v49, v37
	v_min_u32_e32 v37, v49, v37
	v_max_u32_e32 v49, v47, v35
	v_max_u32_e32 v74, v61, v53
	v_min_u32_e32 v53, v61, v53
	v_max_u32_e32 v61, v59, v51
	v_xor_b32_e32 v63, v63, v75
	v_xor_b32_e32 v64, v64, v76
	v_xor_b32_e32 v65, v65, v77
	v_min_u32_e32 v35, v47, v35
	v_max_u32_e32 v47, v49, v37
	v_min_u32_e32 v37, v49, v37
	v_max_u32_e32 v49, v48, v36
	v_min_u32_e32 v36, v48, v36
	v_max_u32_e32 v48, v46, v34
	v_min_u32_e32 v51, v59, v51
	v_max_u32_e32 v59, v61, v53
	v_min_u32_e32 v53, v61, v53
	v_max_u32_e32 v61, v60, v52
	v_min_u32_e32 v52, v60, v52
	v_max_u32_e32 v60, v58, v50
	v_and_or_b32 v62, v62, s53, v115
	v_and_or_b32 v39, v39, s53, v116
	v_and_or_b32 v63, v63, s53, v117
	v_and_or_b32 v40, v40, s53, v118
	v_and_or_b32 v64, v64, s53, v119
	v_and_or_b32 v41, v41, s53, v120
	v_and_or_b32 v65, v65, s53, v121
	v_min_u32_e32 v34, v46, v34
	v_max_u32_e32 v46, v48, v36
	v_min_u32_e32 v36, v48, v36
	v_min_u32_e32 v50, v58, v50
	v_max_u32_e32 v58, v60, v52
	v_min_u32_e32 v52, v60, v52
	v_max_u32_e32 v48, v49, v47
	v_min_u32_e32 v47, v49, v47
	v_max_u32_e32 v49, v46, v37
	v_min_u32_e32 v37, v46, v37
	v_max_u32_e32 v46, v36, v35
	v_min_u32_e32 v35, v36, v35
	v_max_u32_e32 v36, v38, v39
	v_min_u32_e32 v38, v38, v39
	v_max_u32_e32 v39, v40, v41
	v_min_u32_e32 v40, v40, v41
	v_max_u32_e32 v60, v61, v59
; __device__ __forceinline__ void topk_phase(LAS unsigned char* lds, const bf16_t* qp, const bf16_t* keys, const float* SU, const float* SV, int* sel_e, float* sel_g, float* sel_su, int G, int b) {
;     ...
;             SN_SORT16(T[p]); SN_SORT16(lo16);
; #pragma unroll
;             for (int i = 0; i < 16; ++i) T[p][i] = umax_(T[p][i], lo16[15 - i]);
;             SN_BITONIC16(T[p]);
	v_min_u32_e32 v59, v61, v59
	v_max_u32_e32 v61, v58, v53
	v_min_u32_e32 v53, v58, v53
	v_max_u32_e32 v58, v52, v51
	v_min_u32_e32 v51, v52, v51
	v_max_u32_e32 v52, v62, v63
	v_min_u32_e32 v62, v62, v63
	v_max_u32_e32 v63, v64, v65
	v_min_u32_e32 v64, v64, v65
	v_and_or_b32 v42, v42, s53, v122
	v_and_or_b32 v54, v54, s53, v123
	v_and_or_b32 v43, v43, s53, v124
	v_and_or_b32 v55, v55, s53, v125
	v_and_or_b32 v44, v44, s53, v126
	v_and_or_b32 v56, v56, s53, v127
	v_and_or_b32 v45, v45, s53, v128
	v_and_or_b32 v57, v57, s53, v129
	v_max_u32_e32 v41, v36, v39
	v_min_u32_e32 v36, v36, v39
	v_max_u32_e32 v39, v38, v40
	v_max_u32_e32 v65, v52, v63
	v_min_u32_e32 v52, v52, v63
	v_max_u32_e32 v63, v62, v64
	v_min_u32_e32 v38, v38, v40
	v_max_u32_e32 v40, v39, v36
	v_min_u32_e32 v36, v39, v36
	v_max_u32_e32 v39, v42, v43
	v_min_u32_e32 v42, v42, v43
	v_max_u32_e32 v43, v44, v45
	v_min_u32_e32 v44, v44, v45
	v_min_u32_e32 v62, v62, v64
	v_max_u32_e32 v64, v63, v52
	v_min_u32_e32 v52, v63, v52
	v_max_u32_e32 v63, v54, v55
	v_min_u32_e32 v54, v54, v55
	v_max_u32_e32 v55, v56, v57
	v_min_u32_e32 v56, v56, v57
	v_max_u32_e32 v45, v39, v43
	v_min_u32_e32 v39, v39, v43
	v_max_u32_e32 v43, v42, v44
	v_max_u32_e32 v57, v63, v55
	v_min_u32_e32 v55, v63, v55
	v_max_u32_e32 v63, v54, v56
	v_min_u32_e32 v42, v42, v44
	v_max_u32_e32 v44, v43, v39
	v_min_u32_e32 v39, v43, v39
	v_min_u32_e32 v54, v54, v56
	v_max_u32_e32 v56, v63, v55
	v_min_u32_e32 v55, v63, v55
	v_max_u32_e32 v43, v41, v45
	v_min_u32_e32 v41, v41, v45
	v_max_u32_e32 v45, v36, v39
	v_max_u32_e32 v63, v65, v57
	v_min_u32_e32 v57, v65, v57
	v_max_u32_e32 v65, v52, v55
	v_min_u32_e32 v36, v36, v39
	v_max_u32_e32 v39, v45, v41
	v_min_u32_e32 v41, v45, v41
	v_max_u32_e32 v45, v40, v44
	v_min_u32_e32 v40, v40, v44
	v_max_u32_e32 v44, v38, v42
	v_min_u32_e32 v52, v52, v55
	v_max_u32_e32 v55, v65, v57
	v_min_u32_e32 v57, v65, v57
	v_max_u32_e32 v65, v64, v56
	v_min_u32_e32 v56, v64, v56
	v_max_u32_e32 v64, v62, v54
	v_min_u32_e32 v38, v38, v42
	v_max_u32_e32 v42, v44, v40
	v_min_u32_e32 v54, v62, v54
	v_max_u32_e32 v62, v64, v56
	v_min_u32_e32 v40, v44, v40
	v_max_u32_e32 v44, v45, v39
	v_min_u32_e32 v39, v45, v39
	v_max_u32_e32 v45, v42, v41
	v_min_u32_e32 v41, v42, v41
	v_min_u32_e32 v56, v64, v56
	v_max_u32_e32 v64, v65, v55
	v_min_u32_e32 v55, v65, v55
	v_max_u32_e32 v65, v62, v57
	v_min_u32_e32 v57, v62, v57
	v_max_u32_e32 v42, v40, v36
	v_min_u32_e32 v36, v40, v36
	v_min_u32_e32 v40, v66, v43
	v_max_u32_e32 v67, v37, v41
	v_max_u32_e32 v62, v56, v52
	v_min_u32_e32 v52, v56, v52
	v_min_u32_e32 v56, v74, v63
	v_max_u32_e32 v75, v53, v57
	v_min_u32_e32 v37, v37, v41
	v_max_u32_e32 v41, v67, v40
	v_min_u32_e32 v40, v67, v40
	v_max_u32_e32 v67, v47, v39
	v_min_u32_e32 v39, v47, v39
	v_max_u32_e32 v47, v35, v36
	v_min_u32_e32 v53, v53, v57
	v_max_u32_e32 v57, v75, v56
	v_min_u32_e32 v56, v75, v56
	v_max_u32_e32 v75, v59, v55
	v_min_u32_e32 v55, v59, v55
	v_max_u32_e32 v59, v51, v52
	v_min_u32_e32 v35, v35, v36
	v_max_u32_e32 v36, v47, v39
	v_min_u32_e32 v39, v47, v39
	v_min_u32_e32 v51, v51, v52
	v_max_u32_e32 v52, v59, v55
	v_min_u32_e32 v55, v59, v55
	v_max_u32_e32 v47, v67, v41
	v_min_u32_e32 v41, v67, v41
	v_max_u32_e32 v67, v36, v40
	v_min_u32_e32 v36, v36, v40
	v_max_u32_e32 v40, v39, v37
	v_min_u32_e32 v37, v39, v37
	v_max_u32_e32 v39, v48, v44
	v_min_u32_e32 v44, v48, v44
	v_max_u32_e32 v48, v46, v42
	v_max_u32_e32 v59, v75, v57
	v_min_u32_e32 v57, v75, v57
	v_max_u32_e32 v75, v52, v56
	v_min_u32_e32 v52, v52, v56
	v_max_u32_e32 v56, v55, v53
	v_min_u32_e32 v53, v55, v53
	v_max_u32_e32 v55, v60, v64
	v_min_u32_e32 v60, v60, v64
	v_max_u32_e32 v64, v58, v62
	v_min_u32_e32 v42, v46, v42
	v_max_u32_e32 v46, v48, v44
	v_min_u32_e32 v44, v48, v44
	v_max_u32_e32 v48, v49, v45
	v_min_u32_e32 v45, v49, v45
	v_max_u32_e32 v49, v34, v38
	v_min_u32_e32 v58, v58, v62
	v_max_u32_e32 v62, v64, v60
	v_min_u32_e32 v60, v64, v60
	v_max_u32_e32 v64, v61, v65
	v_min_u32_e32 v61, v61, v65
	v_max_u32_e32 v65, v50, v54
	v_min_u32_e32 v34, v34, v38
	v_max_u32_e32 v38, v49, v45
	v_min_u32_e32 v45, v49, v45
	v_min_u32_e32 v50, v50, v54
	v_max_u32_e32 v54, v65, v61
	v_min_u32_e32 v61, v65, v61
	v_max_u32_e32 v49, v48, v46
	v_min_u32_e32 v46, v48, v46
	v_max_u32_e32 v48, v38, v44
	v_min_u32_e32 v38, v38, v44
	v_max_u32_e32 v44, v45, v42
	v_min_u32_e32 v42, v45, v42
	v_max_u32_e32 v65, v64, v62
	v_min_u32_e32 v62, v64, v62
	v_max_u32_e32 v64, v54, v60
	v_min_u32_e32 v54, v54, v60
	v_max_u32_e32 v60, v61, v58
	v_min_u32_e32 v58, v61, v58
	v_min_u32_e32 v45, v39, v47
	v_min_u32_e32 v68, v49, v41
	v_min_u32_e32 v69, v46, v67
	v_min_u32_e32 v70, v48, v36
	v_min_u32_e32 v71, v38, v40
	v_min_u32_e32 v72, v44, v37
	v_min_u32_e32 v73, v42, v35
	v_min_u32_e32 v61, v55, v59
	v_min_u32_e32 v76, v65, v57
	v_min_u32_e32 v77, v62, v75
	v_min_u32_e32 v134, v64, v52
	v_min_u32_e32 v135, v54, v56
	v_min_u32_e32 v136, v60, v53
	v_min_u32_e32 v137, v58, v51
	v_max3_u32 v43, v66, v43, v50
	v_max3_u32 v39, v39, v47, v137
	v_max3_u32 v45, v45, v58, v51
	v_max3_u32 v41, v49, v41, v136
	v_max3_u32 v47, v68, v60, v53
	v_max3_u32 v46, v46, v67, v135
	v_max3_u32 v49, v69, v54, v56
	v_max3_u32 v36, v48, v36, v134
	v_max3_u32 v48, v70, v64, v52
	v_max3_u32 v38, v38, v40, v77
	v_max3_u32 v40, v71, v62, v75
	v_max3_u32 v37, v44, v37, v76
	v_max3_u32 v44, v72, v65, v57
	v_max3_u32 v35, v42, v35, v61
	v_max3_u32 v42, v73, v55, v59
	v_max3_u32 v34, v34, v74, v63
	v_max_u32_e32 v50, v43, v48
	v_min_u32_e32 v43, v43, v48
	v_max_u32_e32 v48, v39, v38
	v_min_u32_e32 v38, v39, v38
	v_max_u32_e32 v39, v45, v40
	v_min_u32_e32 v40, v45, v40
	v_max_u32_e32 v45, v41, v37
; #define LAS __attribute__((address_space(3)))
; __device__ __forceinline__ f32x4 mfma16(bf16x8 a, bf16x8 b, f32x4 c) { return __builtin_amdgcn_mfma_f32_16x16x32_bf16(a, b, c, 0, 0, 0); }
; __device__ __forceinline__ void topk_phase(LAS unsigned char* lds, const bf16_t* qp, const bf16_t* keys, const float* SU, const float* SV, int* sel_e, float* sel_g, float* sel_su, int G, int b) {
;     ...
;         for (int p = 0; p < 2; ++p) {
;             f32x4 acc[8];
; #pragma unroll
;             for (int mt = 0; mt < 8; ++mt) acc[mt] = (f32x4){0.f, 0.f, 0.f, 0.f};
;             bf16x8 bq[4];
; #pragma unroll
;             for (int ks = 0; ks < 4; ++ks) bq[ks] = *(const bf16x8*)(qp + (size_t)tok * D_ + h * 256 + p * 128 + ks * 32 + fq * 8);
;             const LAS bf16_t* kb = KL + p * 128 * 136;
; #pragma unroll
;             for (int mt = 0; mt < 8; ++mt)
; #pragma unroll
;                 for (int ks = 0; ks < 4; ++ks) { const bf16x8 a = *(const LAS bf16x8*)(kb + (mt * 16 + fr) * 136 + ks * 32 + fq * 8); acc[mt] = mfma16(a, bq[ks], acc[mt]); }
;     ...
;             SN_BITONIC16(T[p]);
;             TOPK_XMERGE(T[p], 16); TOPK_XMERGE(T[p], 32);
	v_min_u32_e32 v37, v41, v37
	v_max_u32_e32 v41, v47, v44
	v_min_u32_e32 v44, v47, v44
	v_max_u32_e32 v47, v46, v35
	v_min_u32_e32 v35, v46, v35
	v_max_u32_e32 v46, v49, v42
	v_min_u32_e32 v42, v49, v42
	v_max_u32_e32 v49, v36, v34
	v_min_u32_e32 v34, v36, v34
	v_max_u32_e32 v36, v50, v41
	v_min_u32_e32 v41, v50, v41
	v_max_u32_e32 v50, v48, v47
	v_min_u32_e32 v47, v48, v47
	v_max_u32_e32 v48, v39, v46
	v_min_u32_e32 v39, v39, v46
	v_max_u32_e32 v46, v45, v49
	v_min_u32_e32 v45, v45, v49
	v_max_u32_e32 v49, v43, v44
	v_min_u32_e32 v43, v43, v44
	v_max_u32_e32 v44, v38, v35
	v_min_u32_e32 v35, v38, v35
	v_max_u32_e32 v38, v40, v42
	v_min_u32_e32 v40, v40, v42
	v_max_u32_e32 v42, v37, v34
	v_min_u32_e32 v34, v37, v34
	v_max_u32_e32 v37, v36, v48
	v_min_u32_e32 v36, v36, v48
	v_max_u32_e32 v48, v50, v46
	v_min_u32_e32 v46, v50, v46
	v_max_u32_e32 v50, v41, v39
	v_min_u32_e32 v39, v41, v39
	v_max_u32_e32 v41, v47, v45
	v_min_u32_e32 v45, v47, v45
	v_max_u32_e32 v47, v49, v38
	v_min_u32_e32 v38, v49, v38
	v_max_u32_e32 v49, v44, v42
	v_min_u32_e32 v42, v44, v42
	v_max_u32_e32 v44, v43, v40
	v_min_u32_e32 v40, v43, v40
	v_max_u32_e32 v43, v35, v34
	v_min_u32_e32 v34, v35, v34
	v_max_u32_e32 v35, v37, v48
	v_min_u32_e32 v37, v37, v48
	v_max_u32_e32 v48, v36, v46
	v_min_u32_e32 v36, v36, v46
	v_max_u32_e32 v46, v50, v41
	v_min_u32_e32 v41, v50, v41
	v_max_u32_e32 v50, v39, v45
	v_min_u32_e32 v39, v39, v45
	v_max_u32_e32 v45, v47, v49
	v_min_u32_e32 v47, v47, v49
	v_max_u32_e32 v49, v38, v42
	v_min_u32_e32 v38, v38, v42
	v_max_u32_e32 v42, v44, v43
	v_min_u32_e32 v43, v44, v43
	v_max_u32_e32 v44, v40, v34
	v_min_u32_e32 v34, v40, v34
	v_mov_b32_e32 v40, v35
	v_mov_b32_e32 v51, v37
	v_mov_b32_e32 v52, v48
	v_mov_b32_e32 v53, v36
	v_mov_b32_e32 v54, v46
	v_mov_b32_e32 v55, v41
	v_mov_b32_e32 v56, v50
	v_mov_b32_e32 v57, v39
	v_mov_b32_e32 v58, v45
	v_mov_b32_e32 v59, v47
	v_mov_b32_e32 v60, v49
	v_mov_b32_e32 v61, v38
	v_mov_b32_e32 v62, v42
	v_mov_b32_e32 v63, v43
	v_mov_b32_e32 v64, v44
	v_mov_b32_e32 v65, v34
	v_permlane16_swap_b32_e32 v35, v40
	v_permlane16_swap_b32_e32 v37, v51
	v_permlane16_swap_b32_e32 v48, v52
	v_permlane16_swap_b32_e32 v36, v53
	v_permlane16_swap_b32_e32 v46, v54
	v_permlane16_swap_b32_e32 v41, v55
	v_permlane16_swap_b32_e32 v50, v56
	v_permlane16_swap_b32_e32 v39, v57
	v_permlane16_swap_b32_e32 v45, v58
	v_permlane16_swap_b32_e32 v47, v59
	v_permlane16_swap_b32_e32 v49, v60
	v_permlane16_swap_b32_e32 v38, v61
	v_permlane16_swap_b32_e32 v42, v62
	v_permlane16_swap_b32_e32 v43, v63
	v_permlane16_swap_b32_e32 v44, v64
	v_permlane16_swap_b32_e32 v34, v65
	v_max_u32_e32 v35, v35, v65
	v_max_u32_e32 v37, v37, v64
	v_max_u32_e32 v48, v48, v63
	v_max_u32_e32 v36, v36, v62
	v_max_u32_e32 v46, v46, v61
	v_max_u32_e32 v41, v41, v60
	v_max_u32_e32 v50, v50, v59
	v_max_u32_e32 v39, v39, v58
	v_max_u32_e32 v45, v45, v57
	v_max_u32_e32 v47, v47, v56
	v_max_u32_e32 v49, v49, v55
	v_max_u32_e32 v38, v38, v54
	v_max_u32_e32 v42, v42, v53
	v_max_u32_e32 v43, v43, v52
	v_max_u32_e32 v44, v44, v51
	v_max_u32_e32 v34, v34, v40
	v_max_u32_e32 v40, v35, v45
	v_min_u32_e32 v35, v35, v45
	v_max_u32_e32 v45, v37, v47
	v_min_u32_e32 v37, v37, v47
	v_max_u32_e32 v47, v48, v49
	v_min_u32_e32 v48, v48, v49
	v_max_u32_e32 v49, v36, v38
	v_min_u32_e32 v36, v36, v38
	v_max_u32_e32 v38, v46, v42
	v_min_u32_e32 v42, v46, v42
	v_max_u32_e32 v46, v41, v43
	v_min_u32_e32 v41, v41, v43
	v_max_u32_e32 v43, v50, v44
	v_min_u32_e32 v44, v50, v44
	v_max_u32_e32 v50, v39, v34
	v_min_u32_e32 v34, v39, v34
	v_max_u32_e32 v39, v40, v38
	v_min_u32_e32 v38, v40, v38
	v_max_u32_e32 v40, v45, v46
	v_min_u32_e32 v45, v45, v46
	v_max_u32_e32 v46, v47, v43
	v_min_u32_e32 v43, v47, v43
	v_max_u32_e32 v47, v49, v50
	v_min_u32_e32 v49, v49, v50
	v_max_u32_e32 v50, v35, v42
	v_min_u32_e32 v35, v35, v42
	v_max_u32_e32 v42, v37, v41
	v_min_u32_e32 v37, v37, v41
	v_max_u32_e32 v41, v48, v44
	v_min_u32_e32 v44, v48, v44
	v_max_u32_e32 v48, v36, v34
	v_min_u32_e32 v34, v36, v34
	v_max_u32_e32 v36, v39, v46
	v_min_u32_e32 v39, v39, v46
	v_max_u32_e32 v46, v40, v47
	v_min_u32_e32 v40, v40, v47
	v_max_u32_e32 v47, v38, v43
	v_min_u32_e32 v38, v38, v43
	v_max_u32_e32 v43, v45, v49
	v_min_u32_e32 v45, v45, v49
	v_max_u32_e32 v49, v50, v41
	v_min_u32_e32 v41, v50, v41
	v_max_u32_e32 v50, v42, v48
	v_min_u32_e32 v42, v42, v48
	v_max_u32_e32 v48, v35, v44
	v_min_u32_e32 v35, v35, v44
	v_max_u32_e32 v44, v37, v34
	v_min_u32_e32 v34, v37, v34
	v_max_u32_e32 v70, v36, v46
	v_min_u32_e32 v71, v36, v46
	v_max_u32_e32 v72, v39, v40
	v_min_u32_e32 v73, v39, v40
	v_max_u32_e32 v74, v47, v43
	v_min_u32_e32 v75, v47, v43
	v_max_u32_e32 v76, v38, v45
	v_min_u32_e32 v77, v38, v45
	v_max_u32_e32 v134, v49, v50
	v_min_u32_e32 v135, v49, v50
	v_max_u32_e32 v136, v41, v42
	v_min_u32_e32 v137, v41, v42
	v_max_u32_e32 v138, v48, v44
	v_min_u32_e32 v139, v48, v44
	v_max_u32_e32 v140, v35, v34
	v_min_u32_e32 v141, v35, v34
	global_load_dwordx4 v[46:49], v[96:97], off offset:256
	global_load_dwordx4 v[42:45], v[96:97], off offset:320
	global_load_dwordx4 v[38:41], v[96:97], off offset:384
	global_load_dwordx4 v[34:37], v[96:97], off offset:448
	ds_read_b128 v[50:53], v131 offset:34816
	ds_read_b128 v[54:57], v131 offset:34880
	s_waitcnt vmcnt(3) lgkmcnt(1)
	v_mfma_f32_16x16x32_bf16 v[50:53], v[50:53], v[46:49], 0
	ds_read_b128 v[58:61], v131 offset:39232
	ds_read_b128 v[62:65], v131 offset:43584
	ds_read_b128 v[66:69], v131 offset:47936
	s_waitcnt vmcnt(2) lgkmcnt(3)
	v_mfma_f32_16x16x32_bf16 v[50:53], v[54:57], v[42:45], v[50:53]
	ds_read_b128 v[54:57], v131 offset:34944
	ds_read_b128 v[158:161], v131 offset:52288
	ds_read_b128 v[162:165], v131 offset:56640
	s_waitcnt vmcnt(1) lgkmcnt(2)
; #define LAS __attribute__((address_space(3)))
; __device__ __forceinline__ f32x4 mfma16(bf16x8 a, bf16x8 b, f32x4 c) { return __builtin_amdgcn_mfma_f32_16x16x32_bf16(a, b, c, 0, 0, 0); }
; __device__ __forceinline__ void topk_phase(LAS unsigned char* lds, const bf16_t* qp, const bf16_t* keys, const float* SU, const float* SV, int* sel_e, float* sel_g, float* sel_su, int G, int b) {
;     ...
; #pragma unroll
;             for (int ks = 0; ks < 4; ++ks) bq[ks] = *(const bf16x8*)(qp + (size_t)tok * D_ + h * 256 + p * 128 + ks * 32 + fq * 8);
;             const LAS bf16_t* kb = KL + p * 128 * 136;
; #pragma unroll
;             for (int mt = 0; mt < 8; ++mt)
; #pragma unroll
;                 for (int ks = 0; ks < 4; ++ks) { const bf16x8 a = *(const LAS bf16x8*)(kb + (mt * 16 + fr) * 136 + ks * 32 + fq * 8); acc[mt] = mfma16(a, bq[ks], acc[mt]); }
	v_mfma_f32_16x16x32_bf16 v[50:53], v[54:57], v[38:41], v[50:53]
	ds_read_b128 v[54:57], v131 offset:35008
	ds_read_b128 v[166:169], v131 offset:60992
	v_mov_b32_e32 v142, v70
	s_waitcnt vmcnt(0) lgkmcnt(1)
	v_mfma_f32_16x16x32_bf16 v[50:53], v[54:57], v[34:37], v[50:53]
	ds_read_b128 v[54:57], v131 offset:39168
	v_mov_b32_e32 v143, v71
	v_mov_b32_e32 v144, v72
	s_waitcnt lgkmcnt(0)
	v_mfma_f32_16x16x32_bf16 v[54:57], v[54:57], v[46:49], 0
	s_nop 2
	v_mov_b32_e32 v145, v73
	v_mov_b32_e32 v146, v74
	v_mfma_f32_16x16x32_bf16 v[54:57], v[58:61], v[42:45], v[54:57]
	ds_read_b128 v[58:61], v131 offset:39296
	v_mov_b32_e32 v147, v75
	v_mov_b32_e32 v148, v76
	s_waitcnt lgkmcnt(0)
	v_mfma_f32_16x16x32_bf16 v[54:57], v[58:61], v[38:41], v[54:57]
	ds_read_b128 v[58:61], v131 offset:39360
	v_mov_b32_e32 v149, v77
	v_mov_b32_e32 v150, v134
	s_waitcnt lgkmcnt(0)
	v_mfma_f32_16x16x32_bf16 v[54:57], v[58:61], v[34:37], v[54:57]
	ds_read_b128 v[58:61], v131 offset:43520
	v_mov_b32_e32 v151, v135
	v_mov_b32_e32 v152, v136
	s_waitcnt lgkmcnt(0)
	v_mfma_f32_16x16x32_bf16 v[58:61], v[58:61], v[46:49], 0
	v_mov_b32_e32 v153, v137
	v_mov_b32_e32 v154, v138
	v_mov_b32_e32 v155, v139
	v_mfma_f32_16x16x32_bf16 v[58:61], v[62:65], v[42:45], v[58:61]
	ds_read_b128 v[62:65], v131 offset:43648
	v_mov_b32_e32 v156, v140
	v_mov_b32_e32 v157, v141
	s_waitcnt lgkmcnt(0)
	v_mfma_f32_16x16x32_bf16 v[58:61], v[62:65], v[38:41], v[58:61]
	ds_read_b128 v[62:65], v131 offset:43712
	v_permlane32_swap_b32_e32 v70, v142
	s_waitcnt lgkmcnt(0)
	v_mfma_f32_16x16x32_bf16 v[58:61], v[62:65], v[34:37], v[58:61]
	ds_read_b128 v[62:65], v131 offset:47872
	v_permlane32_swap_b32_e32 v71, v143
	s_waitcnt lgkmcnt(0)
	v_mfma_f32_16x16x32_bf16 v[62:65], v[62:65], v[46:49], 0
	v_permlane32_swap_b32_e32 v72, v144
	v_permlane32_swap_b32_e32 v73, v145
	v_mfma_f32_16x16x32_bf16 v[62:65], v[66:69], v[42:45], v[62:65]
	ds_read_b128 v[66:69], v131 offset:48000
	v_permlane32_swap_b32_e32 v74, v146
	s_waitcnt lgkmcnt(0)
	v_mfma_f32_16x16x32_bf16 v[62:65], v[66:69], v[38:41], v[62:65]
	ds_read_b128 v[66:69], v131 offset:48064
	v_permlane32_swap_b32_e32 v75, v147
	s_waitcnt lgkmcnt(0)
	v_mfma_f32_16x16x32_bf16 v[62:65], v[66:69], v[34:37], v[62:65]
	ds_read_b128 v[66:69], v131 offset:52224
	v_permlane32_swap_b32_e32 v76, v148
	s_waitcnt lgkmcnt(0)
	v_mfma_f32_16x16x32_bf16 v[66:69], v[66:69], v[46:49], 0
	v_permlane32_swap_b32_e32 v77, v149
	v_permlane32_swap_b32_e32 v134, v150
	v_mfma_f32_16x16x32_bf16 v[66:69], v[158:161], v[42:45], v[66:69]
	ds_read_b128 v[158:161], v131 offset:52352
	v_permlane32_swap_b32_e32 v135, v151
	s_waitcnt lgkmcnt(0)
	v_mfma_f32_16x16x32_bf16 v[66:69], v[158:161], v[38:41], v[66:69]
	ds_read_b128 v[158:161], v131 offset:52416
	v_permlane32_swap_b32_e32 v136, v152
	s_waitcnt lgkmcnt(0)
	v_mfma_f32_16x16x32_bf16 v[66:69], v[158:161], v[34:37], v[66:69]
	ds_read_b128 v[158:161], v131 offset:56576
	v_permlane32_swap_b32_e32 v137, v153
	s_waitcnt lgkmcnt(0)
	v_mfma_f32_16x16x32_bf16 v[158:161], v[158:161], v[46:49], 0
	v_permlane32_swap_b32_e32 v138, v154
	v_permlane32_swap_b32_e32 v139, v155
	v_mfma_f32_16x16x32_bf16 v[158:161], v[162:165], v[42:45], v[158:161]
	ds_read_b128 v[162:165], v131 offset:56704
	v_permlane32_swap_b32_e32 v140, v156
	s_waitcnt lgkmcnt(0)
	v_mfma_f32_16x16x32_bf16 v[158:161], v[162:165], v[38:41], v[158:161]
	ds_read_b128 v[162:165], v131 offset:56768
	v_permlane32_swap_b32_e32 v141, v157
	s_waitcnt lgkmcnt(0)
	v_mfma_f32_16x16x32_bf16 v[158:161], v[162:165], v[34:37], v[158:161]
	ds_read_b128 v[162:165], v131 offset:60928
	s_waitcnt lgkmcnt(0)
	v_mfma_f32_16x16x32_bf16 v[162:165], v[162:165], v[46:49], 0
	v_mfma_f32_16x16x32_bf16 v[162:165], v[166:169], v[42:45], v[162:165]
	ds_read_b128 v[166:169], v131 offset:61056
	s_waitcnt lgkmcnt(0)
	v_mfma_f32_16x16x32_bf16 v[162:165], v[166:169], v[38:41], v[162:165]
	ds_read_b128 v[166:169], v131 offset:61120
	s_waitcnt lgkmcnt(0)
	v_mfma_f32_16x16x32_bf16 v[162:165], v[166:169], v[34:37], v[162:165]
	ds_read_b128 v[166:169], v131 offset:65280
	s_waitcnt lgkmcnt(0)
	v_mfma_f32_16x16x32_bf16 v[46:49], v[166:169], v[46:49], 0
	ds_read_b128 v[166:169], v131 offset:65344
	s_waitcnt lgkmcnt(0)
	v_mfma_f32_16x16x32_bf16 v[42:45], v[166:169], v[42:45], v[46:49]
	s_nop 4
	ds_read_b128 v[46:49], v131 offset:65408
	s_waitcnt lgkmcnt(0)
	v_mfma_f32_16x16x32_bf16 v[38:41], v[46:49], v[38:41], v[42:45]
	s_nop 2
	ds_read_b128 v[42:45], v131 offset:65472
	s_waitcnt lgkmcnt(0)
; #define LAS __attribute__((address_space(3)))
; __device__ __forceinline__ f32x4 mfma16(bf16x8 a, bf16x8 b, f32x4 c) { return __builtin_amdgcn_mfma_f32_16x16x32_bf16(a, b, c, 0, 0, 0); }
; __device__ __forceinline__ unsigned mono(float f) { const unsigned u = __float_as_uint(f); return (u & 0x80000000u) ? ~u : (u ^ 0x80000000u); }
; __device__ __forceinline__ void topk_phase(LAS unsigned char* lds, const bf16_t* qp, const bf16_t* keys, const float* SU, const float* SV, int* sel_e, float* sel_g, float* sel_su, int G, int b) {
;     ...
;                 for (int ks = 0; ks < 4; ++ks) { const bf16x8 a = *(const LAS bf16x8*)(kb + (mt * 16 + fr) * 136 + ks * 32 + fq * 8); acc[mt] = mfma16(a, bq[ks], acc[mt]); }
;             unsigned lo16[16];
; #pragma unroll
;             for (int mt = 0; mt < 4; ++mt)
; #pragma unroll
;                 for (int r = 0; r < 4; ++r) {
;                     T[p][mt * 4 + r] = (mono(acc[mt][r]) & ~127u) | (unsigned)(127 - (mt * 16 + fq * 4 + r));
;                     lo16[mt * 4 + r] = (mono(acc[mt + 4][r]) & ~127u) | (unsigned)(127 - ((mt + 4) * 16 + fq * 4 + r));
;                 }
;             SN_SORT16(T[p]); SN_SORT16(lo16);
	v_mfma_f32_16x16x32_bf16 v[34:37], v[42:45], v[34:37], v[38:41]
	s_nop 2
	v_ashrrev_i32_e32 v38, 31, v50
	v_bitop3_b32 v38, v50, v38, v132 bitop3:0x1e
	v_and_or_b32 v38, v38, s53, v98
	v_ashrrev_i32_e32 v39, 31, v66
	v_bitop3_b32 v39, v66, v39, v132 bitop3:0x1e
	v_and_or_b32 v39, v39, s53, v99
	v_ashrrev_i32_e32 v40, 31, v51
	v_bitop3_b32 v40, v51, v40, v132 bitop3:0x1e
	v_and_or_b32 v40, v40, s53, v100
	v_ashrrev_i32_e32 v41, 31, v67
	v_bitop3_b32 v41, v67, v41, v132 bitop3:0x1e
	v_and_or_b32 v41, v41, s53, v101
	v_ashrrev_i32_e32 v42, 31, v52
	v_bitop3_b32 v42, v52, v42, v132 bitop3:0x1e
	v_and_or_b32 v42, v42, s53, v102
	v_ashrrev_i32_e32 v43, 31, v68
	v_bitop3_b32 v43, v68, v43, v132 bitop3:0x1e
	v_and_or_b32 v43, v43, s53, v103
	v_ashrrev_i32_e32 v44, 31, v53
	v_bitop3_b32 v44, v53, v44, v132 bitop3:0x1e
	v_and_or_b32 v44, v44, s53, v104
	v_ashrrev_i32_e32 v45, 31, v69
	v_bitop3_b32 v45, v69, v45, v132 bitop3:0x1e
	v_and_or_b32 v45, v45, s53, v105
	v_ashrrev_i32_e32 v46, 31, v54
	v_bitop3_b32 v46, v54, v46, v132 bitop3:0x1e
	v_and_or_b32 v46, v46, s53, v106
	v_ashrrev_i32_e32 v47, 31, v158
	v_bitop3_b32 v47, v158, v47, v132 bitop3:0x1e
	v_and_or_b32 v47, v47, s53, v107
	v_ashrrev_i32_e32 v48, 31, v55
	v_bitop3_b32 v48, v55, v48, v132 bitop3:0x1e
	v_and_or_b32 v48, v48, s53, v108
	v_ashrrev_i32_e32 v49, 31, v159
	v_bitop3_b32 v49, v159, v49, v132 bitop3:0x1e
	v_and_or_b32 v49, v49, s53, v109
	v_ashrrev_i32_e32 v50, 31, v56
	v_bitop3_b32 v50, v56, v50, v132 bitop3:0x1e
	v_and_or_b32 v50, v50, s53, v110
	v_ashrrev_i32_e32 v51, 31, v160
	v_bitop3_b32 v51, v160, v51, v132 bitop3:0x1e
	v_max_u32_e32 v160, v39, v41
	v_ashrrev_i32_e32 v52, 31, v57
	v_bitop3_b32 v52, v57, v52, v132 bitop3:0x1e
	v_min_u32_e32 v39, v39, v41
	v_ashrrev_i32_e32 v53, 31, v161
	v_bitop3_b32 v53, v161, v53, v132 bitop3:0x1e
	v_max_u32_e32 v41, v43, v45
	v_ashrrev_i32_e32 v54, 31, v58
	v_cmp_lt_i32_e32 vcc, -1, v162
	v_bitop3_b32 v54, v58, v54, v132 bitop3:0x1e
	v_min_u32_e32 v43, v43, v45
	v_cndmask_b32_e32 v55, -1, v132, vcc
	v_and_or_b32 v51, v51, s53, v111
	v_and_or_b32 v52, v52, s53, v112
	v_ashrrev_i32_e32 v56, 31, v59
	v_cmp_lt_i32_e32 vcc, -1, v163
	v_bitop3_b32 v56, v59, v56, v132 bitop3:0x1e
	v_and_or_b32 v53, v53, s53, v113
	v_cndmask_b32_e32 v57, -1, v132, vcc
	v_max_u32_e32 v45, v160, v41
	v_min_u32_e32 v41, v160, v41
	v_ashrrev_i32_e32 v58, 31, v60
	v_cmp_lt_i32_e32 vcc, -1, v164
	v_bitop3_b32 v58, v60, v58, v132 bitop3:0x1e
	v_max_u32_e32 v160, v39, v43
	v_cndmask_b32_e32 v59, -1, v132, vcc
	v_min_u32_e32 v39, v39, v43
	v_max_u32_e32 v43, v160, v41
	v_ashrrev_i32_e32 v60, 31, v61
	v_cmp_lt_i32_e32 vcc, -1, v165
	v_bitop3_b32 v60, v61, v60, v132 bitop3:0x1e
	v_min_u32_e32 v41, v160, v41
	v_cndmask_b32_e32 v61, -1, v132, vcc
	v_max_u32_e32 v160, v47, v49
	v_min_u32_e32 v47, v47, v49
	v_ashrrev_i32_e32 v66, 31, v62
	v_bitop3_b32 v62, v62, v66, v132 bitop3:0x1e
	v_max_u32_e32 v49, v51, v53
	v_ashrrev_i32_e32 v66, 31, v34
	v_bitop3_b32 v34, v34, v66, v132 bitop3:0x1e
	v_min_u32_e32 v51, v51, v53
	v_ashrrev_i32_e32 v66, 31, v63
	v_bitop3_b32 v63, v63, v66, v132 bitop3:0x1e
	v_max_u32_e32 v53, v160, v49
	v_ashrrev_i32_e32 v66, 31, v35
	v_bitop3_b32 v35, v35, v66, v132 bitop3:0x1e
	v_min_u32_e32 v49, v160, v49
	v_ashrrev_i32_e32 v66, 31, v64
	v_bitop3_b32 v64, v64, v66, v132 bitop3:0x1e
	v_max_u32_e32 v160, v47, v51
	v_ashrrev_i32_e32 v66, 31, v36
	v_bitop3_b32 v36, v36, v66, v132 bitop3:0x1e
	v_min_u32_e32 v47, v47, v51
	v_ashrrev_i32_e32 v66, 31, v65
	v_cmp_lt_i32_e32 vcc, -1, v37
	v_bitop3_b32 v65, v65, v66, v132 bitop3:0x1e
	v_max_u32_e32 v51, v160, v49
	v_cndmask_b32_e32 v66, -1, v132, vcc
	v_xor_b32_e32 v37, v66, v37
	v_max_u32_e32 v66, v38, v40
	v_min_u32_e32 v38, v38, v40
	v_max_u32_e32 v40, v42, v44
	v_min_u32_e32 v42, v42, v44
	v_max_u32_e32 v44, v66, v40
	v_min_u32_e32 v40, v66, v40
	v_max_u32_e32 v66, v38, v42
	v_min_u32_e32 v38, v38, v42
	v_max_u32_e32 v42, v66, v40
	v_min_u32_e32 v40, v66, v40
	v_max_u32_e32 v66, v46, v48
	v_min_u32_e32 v46, v46, v48
	v_max_u32_e32 v48, v50, v52
	v_min_u32_e32 v50, v50, v52
	v_max_u32_e32 v52, v66, v48
	v_min_u32_e32 v48, v66, v48
	v_max_u32_e32 v66, v46, v50
	v_min_u32_e32 v46, v46, v50
	v_max_u32_e32 v50, v66, v48
	v_min_u32_e32 v48, v66, v48
	v_min_u32_e32 v49, v160, v49
	v_max_u32_e32 v66, v44, v52
	v_min_u32_e32 v44, v44, v52
	v_max_u32_e32 v52, v40, v48
	v_max_u32_e32 v160, v45, v53
	v_min_u32_e32 v45, v45, v53
	v_max_u32_e32 v53, v41, v49
	v_xor_b32_e32 v55, v55, v162
	v_xor_b32_e32 v57, v57, v163
	v_xor_b32_e32 v59, v59, v164
	v_xor_b32_e32 v61, v61, v165
	v_min_u32_e32 v40, v40, v48
	v_max_u32_e32 v48, v52, v44
	v_min_u32_e32 v44, v52, v44
	v_max_u32_e32 v52, v42, v50
	v_min_u32_e32 v42, v42, v50
	v_max_u32_e32 v50, v38, v46
	v_min_u32_e32 v41, v41, v49
	v_max_u32_e32 v49, v53, v45
	v_min_u32_e32 v45, v53, v45
	v_max_u32_e32 v53, v43, v51
	v_min_u32_e32 v43, v43, v51
	v_max_u32_e32 v51, v39, v47
	v_and_or_b32 v54, v54, s53, v114
	v_and_or_b32 v55, v55, s53, v115
	v_and_or_b32 v56, v56, s53, v116
	v_and_or_b32 v57, v57, s53, v117
	v_and_or_b32 v58, v58, s53, v118
	v_and_or_b32 v59, v59, s53, v119
	v_and_or_b32 v60, v60, s53, v120
	v_and_or_b32 v61, v61, s53, v121
	v_min_u32_e32 v38, v38, v46
	v_max_u32_e32 v46, v50, v42
	v_min_u32_e32 v42, v50, v42
	v_min_u32_e32 v39, v39, v47
	v_max_u32_e32 v47, v51, v43
	v_min_u32_e32 v43, v51, v43
	v_max_u32_e32 v50, v52, v48
	v_min_u32_e32 v48, v52, v48
	v_max_u32_e32 v52, v46, v44
	v_min_u32_e32 v44, v46, v44
	v_max_u32_e32 v46, v42, v40
	v_min_u32_e32 v40, v42, v40
	v_max_u32_e32 v42, v54, v56
	v_min_u32_e32 v54, v54, v56
	v_max_u32_e32 v56, v58, v60
; __device__ __forceinline__ void topk_phase(LAS unsigned char* lds, const bf16_t* qp, const bf16_t* keys, const float* SU, const float* SV, int* sel_e, float* sel_g, float* sel_su, int G, int b) {
;     ...
;             SN_SORT16(T[p]); SN_SORT16(lo16);
; #pragma unroll
;             for (int i = 0; i < 16; ++i) T[p][i] = umax_(T[p][i], lo16[15 - i]);
;             SN_BITONIC16(T[p]);
	v_min_u32_e32 v58, v58, v60
	v_max_u32_e32 v51, v53, v49
	v_min_u32_e32 v49, v53, v49
	v_max_u32_e32 v53, v47, v45
	v_min_u32_e32 v45, v47, v45
	v_max_u32_e32 v47, v43, v41
	v_min_u32_e32 v41, v43, v41
	v_max_u32_e32 v43, v55, v57
	v_min_u32_e32 v55, v55, v57
	v_max_u32_e32 v57, v59, v61
	v_min_u32_e32 v59, v59, v61
	v_and_or_b32 v62, v62, s53, v122
	v_and_or_b32 v34, v34, s53, v123
	v_and_or_b32 v63, v63, s53, v124
	v_and_or_b32 v35, v35, s53, v125
	v_and_or_b32 v64, v64, s53, v126
	v_and_or_b32 v36, v36, s53, v127
	v_and_or_b32 v65, v65, s53, v128
	v_and_or_b32 v37, v37, s53, v129
	v_max_u32_e32 v60, v42, v56
	v_min_u32_e32 v42, v42, v56
	v_max_u32_e32 v56, v54, v58
	v_max_u32_e32 v61, v43, v57
	v_min_u32_e32 v43, v43, v57
	v_max_u32_e32 v57, v55, v59
	v_min_u32_e32 v54, v54, v58
	v_max_u32_e32 v58, v56, v42
	v_min_u32_e32 v42, v56, v42
	v_max_u32_e32 v56, v62, v63
	v_min_u32_e32 v62, v62, v63
	v_max_u32_e32 v63, v64, v65
	v_min_u32_e32 v64, v64, v65
	v_min_u32_e32 v55, v55, v59
	v_max_u32_e32 v59, v57, v43
	v_min_u32_e32 v43, v57, v43
	v_max_u32_e32 v57, v34, v35
	v_min_u32_e32 v34, v34, v35
	v_max_u32_e32 v35, v36, v37
	v_min_u32_e32 v36, v36, v37
	v_max_u32_e32 v65, v56, v63
	v_min_u32_e32 v56, v56, v63
	v_max_u32_e32 v63, v62, v64
	v_max_u32_e32 v37, v57, v35
	v_min_u32_e32 v35, v57, v35
	v_max_u32_e32 v57, v34, v36
	v_min_u32_e32 v62, v62, v64
	v_max_u32_e32 v64, v63, v56
	v_min_u32_e32 v56, v63, v56
	v_min_u32_e32 v34, v34, v36
	v_max_u32_e32 v36, v57, v35
	v_min_u32_e32 v35, v57, v35
	v_max_u32_e32 v63, v60, v65
	v_min_u32_e32 v60, v60, v65
	v_max_u32_e32 v65, v42, v56
	v_max_u32_e32 v57, v61, v37
	v_min_u32_e32 v37, v61, v37
	v_max_u32_e32 v61, v43, v35
	v_min_u32_e32 v42, v42, v56
	v_max_u32_e32 v56, v65, v60
	v_min_u32_e32 v60, v65, v60
	v_max_u32_e32 v65, v58, v64
	v_min_u32_e32 v58, v58, v64
	v_max_u32_e32 v64, v54, v62
	v_min_u32_e32 v35, v43, v35
	v_max_u32_e32 v43, v61, v37
	v_min_u32_e32 v37, v61, v37
	v_max_u32_e32 v61, v59, v36
	v_min_u32_e32 v36, v59, v36
	v_max_u32_e32 v59, v55, v34
	v_min_u32_e32 v54, v54, v62
	v_max_u32_e32 v62, v64, v58
	v_min_u32_e32 v34, v55, v34
	v_max_u32_e32 v55, v59, v36
	v_min_u32_e32 v58, v64, v58
	v_max_u32_e32 v64, v65, v56
	v_min_u32_e32 v56, v65, v56
	v_max_u32_e32 v65, v62, v60
	v_min_u32_e32 v60, v62, v60
	v_min_u32_e32 v36, v59, v36
	v_max_u32_e32 v59, v61, v43
	v_min_u32_e32 v43, v61, v43
	v_max_u32_e32 v61, v55, v37
	v_min_u32_e32 v37, v55, v37
	v_max_u32_e32 v62, v58, v42
	v_min_u32_e32 v42, v58, v42
	v_min_u32_e32 v58, v66, v63
	v_max_u32_e32 v67, v44, v60
	v_max_u32_e32 v55, v36, v35
	v_min_u32_e32 v35, v36, v35
	v_min_u32_e32 v36, v160, v57
	v_max_u32_e32 v161, v45, v37
	v_min_u32_e32 v44, v44, v60
	v_max_u32_e32 v60, v67, v58
	v_min_u32_e32 v58, v67, v58
	v_max_u32_e32 v67, v48, v56
	v_min_u32_e32 v48, v48, v56
	v_max_u32_e32 v56, v40, v42
	v_min_u32_e32 v37, v45, v37
	v_max_u32_e32 v45, v161, v36
	v_min_u32_e32 v36, v161, v36
	v_max_u32_e32 v161, v49, v43
	v_min_u32_e32 v43, v49, v43
	v_max_u32_e32 v49, v41, v35
	v_min_u32_e32 v40, v40, v42
	v_max_u32_e32 v42, v56, v48
	v_min_u32_e32 v48, v56, v48
	v_min_u32_e32 v35, v41, v35
	v_max_u32_e32 v41, v49, v43
	v_min_u32_e32 v43, v49, v43
	v_max_u32_e32 v56, v67, v60
	v_min_u32_e32 v60, v67, v60
	v_max_u32_e32 v67, v42, v58
	v_min_u32_e32 v42, v42, v58
	v_max_u32_e32 v58, v48, v44
	v_min_u32_e32 v44, v48, v44
	v_max_u32_e32 v48, v50, v64
	v_min_u32_e32 v50, v50, v64
	v_max_u32_e32 v64, v46, v62
	v_max_u32_e32 v49, v161, v45
	v_min_u32_e32 v45, v161, v45
	v_max_u32_e32 v161, v41, v36
	v_min_u32_e32 v36, v41, v36
	v_max_u32_e32 v41, v43, v37
	v_min_u32_e32 v37, v43, v37
	v_max_u32_e32 v43, v51, v59
	v_min_u32_e32 v51, v51, v59
	v_max_u32_e32 v59, v47, v55
	v_min_u32_e32 v46, v46, v62
	v_max_u32_e32 v62, v64, v50
	v_min_u32_e32 v50, v64, v50
	v_max_u32_e32 v64, v52, v65
	v_min_u32_e32 v52, v52, v65
	v_max_u32_e32 v65, v38, v54
	v_min_u32_e32 v47, v47, v55
	v_max_u32_e32 v55, v59, v51
	v_min_u32_e32 v51, v59, v51
	v_max_u32_e32 v59, v53, v61
	v_min_u32_e32 v53, v53, v61
	v_max_u32_e32 v61, v39, v34
	v_min_u32_e32 v38, v38, v54
	v_max_u32_e32 v54, v65, v52
	v_min_u32_e32 v52, v65, v52
	v_min_u32_e32 v34, v39, v34
	v_max_u32_e32 v39, v61, v53
	v_min_u32_e32 v53, v61, v53
	v_max_u32_e32 v65, v64, v62
	v_min_u32_e32 v62, v64, v62
	v_max_u32_e32 v64, v54, v50
	v_min_u32_e32 v50, v54, v50
	v_max_u32_e32 v54, v52, v46
	v_min_u32_e32 v46, v52, v46
	v_max_u32_e32 v61, v59, v55
	v_min_u32_e32 v55, v59, v55
	v_max_u32_e32 v59, v39, v51
	v_min_u32_e32 v39, v39, v51
	v_max_u32_e32 v51, v53, v47
	v_min_u32_e32 v47, v53, v47
	v_min_u32_e32 v52, v48, v56
	v_min_u32_e32 v68, v65, v60
	v_min_u32_e32 v69, v62, v67
	v_min_u32_e32 v96, v64, v42
	v_min_u32_e32 v97, v50, v58
	v_min_u32_e32 v158, v54, v44
	v_min_u32_e32 v159, v46, v40
	v_min_u32_e32 v53, v43, v49
	v_min_u32_e32 v162, v61, v45
	v_min_u32_e32 v163, v55, v161
	v_min_u32_e32 v164, v59, v36
	v_min_u32_e32 v165, v39, v41
	v_min_u32_e32 v166, v51, v37
	v_min_u32_e32 v167, v47, v35
	v_max3_u32 v34, v66, v63, v34
	v_max3_u32 v48, v48, v56, v167
	v_max3_u32 v35, v52, v47, v35
	v_max3_u32 v47, v65, v60, v166
	v_max3_u32 v37, v68, v51, v37
	v_max3_u32 v51, v62, v67, v165
	v_max3_u32 v39, v69, v39, v41
	v_max3_u32 v41, v64, v42, v164
	v_max3_u32 v36, v96, v59, v36
	v_max3_u32 v42, v50, v58, v163
	v_max3_u32 v50, v97, v55, v161
	v_max3_u32 v44, v54, v44, v162
	v_max3_u32 v45, v158, v61, v45
	v_max3_u32 v40, v46, v40, v53
	v_max3_u32 v43, v159, v43, v49
	v_max3_u32 v38, v38, v160, v57
	v_max_u32_e32 v46, v34, v36
	v_min_u32_e32 v34, v34, v36
	v_max_u32_e32 v36, v48, v42
	v_min_u32_e32 v42, v48, v42
; __device__ __forceinline__ void topk_phase(LAS unsigned char* lds, const bf16_t* qp, const bf16_t* keys, const float* SU, const float* SV, int* sel_e, float* sel_g, float* sel_su, int G, int b) {
;     ...
;             SN_BITONIC16(T[p]);
;             TOPK_XMERGE(T[p], 16); TOPK_XMERGE(T[p], 32);
	v_max_u32_e32 v48, v35, v50
	v_min_u32_e32 v35, v35, v50
	v_max_u32_e32 v49, v47, v44
	v_min_u32_e32 v44, v47, v44
	v_max_u32_e32 v47, v37, v45
	v_min_u32_e32 v37, v37, v45
	v_max_u32_e32 v45, v51, v40
	v_min_u32_e32 v40, v51, v40
	v_max_u32_e32 v50, v39, v43
	v_min_u32_e32 v39, v39, v43
	v_max_u32_e32 v43, v41, v38
	v_min_u32_e32 v38, v41, v38
	v_max_u32_e32 v41, v46, v47
	v_min_u32_e32 v46, v46, v47
	v_max_u32_e32 v47, v36, v45
	v_min_u32_e32 v36, v36, v45
	v_max_u32_e32 v45, v48, v50
	v_min_u32_e32 v48, v48, v50
	v_max_u32_e32 v50, v49, v43
	v_min_u32_e32 v43, v49, v43
	v_max_u32_e32 v49, v34, v37
	v_min_u32_e32 v34, v34, v37
	v_max_u32_e32 v37, v42, v40
	v_min_u32_e32 v40, v42, v40
	v_max_u32_e32 v42, v35, v39
	v_min_u32_e32 v35, v35, v39
	v_max_u32_e32 v39, v44, v38
	v_min_u32_e32 v38, v44, v38
	v_max_u32_e32 v44, v41, v45
	v_min_u32_e32 v41, v41, v45
	v_max_u32_e32 v45, v47, v50
	v_min_u32_e32 v47, v47, v50
	v_max_u32_e32 v50, v46, v48
	v_min_u32_e32 v46, v46, v48
	v_max_u32_e32 v48, v36, v43
	v_min_u32_e32 v36, v36, v43
	v_max_u32_e32 v43, v49, v42
	v_min_u32_e32 v42, v49, v42
	v_max_u32_e32 v49, v37, v39
	v_min_u32_e32 v37, v37, v39
	v_max_u32_e32 v39, v34, v35
	v_min_u32_e32 v34, v34, v35
	v_max_u32_e32 v35, v40, v38
	v_min_u32_e32 v38, v40, v38
	v_max_u32_e32 v40, v44, v45
	v_min_u32_e32 v44, v44, v45
	v_max_u32_e32 v45, v41, v47
	v_min_u32_e32 v41, v41, v47
	v_max_u32_e32 v47, v50, v48
	v_min_u32_e32 v48, v50, v48
	v_max_u32_e32 v50, v46, v36
	v_min_u32_e32 v36, v46, v36
	v_max_u32_e32 v46, v43, v49
	v_min_u32_e32 v43, v43, v49
	v_max_u32_e32 v49, v42, v37
	v_min_u32_e32 v37, v42, v37
	v_max_u32_e32 v42, v39, v35
	v_min_u32_e32 v35, v39, v35
	v_max_u32_e32 v39, v34, v38
	v_min_u32_e32 v34, v34, v38
	v_mov_b32_e32 v38, v40
	v_mov_b32_e32 v51, v44
	v_mov_b32_e32 v52, v45
	v_mov_b32_e32 v53, v41
	v_mov_b32_e32 v54, v47
	v_mov_b32_e32 v55, v48
	v_mov_b32_e32 v56, v50
	v_mov_b32_e32 v57, v36
	v_mov_b32_e32 v58, v46
	v_mov_b32_e32 v59, v43
	v_mov_b32_e32 v60, v49
	v_mov_b32_e32 v61, v37
	v_mov_b32_e32 v62, v42
	v_mov_b32_e32 v63, v35
	v_mov_b32_e32 v64, v39
	v_mov_b32_e32 v65, v34
	v_permlane16_swap_b32_e32 v40, v38
	v_permlane16_swap_b32_e32 v44, v51
	v_permlane16_swap_b32_e32 v45, v52
	v_permlane16_swap_b32_e32 v41, v53
	v_permlane16_swap_b32_e32 v47, v54
	v_permlane16_swap_b32_e32 v48, v55
	v_permlane16_swap_b32_e32 v50, v56
	v_permlane16_swap_b32_e32 v36, v57
	v_permlane16_swap_b32_e32 v46, v58
	v_permlane16_swap_b32_e32 v43, v59
	v_permlane16_swap_b32_e32 v49, v60
	v_permlane16_swap_b32_e32 v37, v61
	v_permlane16_swap_b32_e32 v42, v62
	v_permlane16_swap_b32_e32 v35, v63
	v_permlane16_swap_b32_e32 v39, v64
	v_permlane16_swap_b32_e32 v34, v65
	v_max_u32_e32 v40, v40, v65
	v_max_u32_e32 v44, v44, v64
	v_max_u32_e32 v45, v45, v63
	v_max_u32_e32 v41, v41, v62
	v_max_u32_e32 v47, v47, v61
	v_max_u32_e32 v48, v48, v60
	v_max_u32_e32 v50, v50, v59
	v_max_u32_e32 v36, v36, v58
	v_max_u32_e32 v46, v46, v57
	v_max_u32_e32 v43, v43, v56
	v_max_u32_e32 v49, v49, v55
	v_max_u32_e32 v37, v37, v54
	v_max_u32_e32 v42, v42, v53
	v_max_u32_e32 v35, v35, v52
	v_max_u32_e32 v39, v39, v51
	v_max_u32_e32 v34, v34, v38
	v_max_u32_e32 v38, v40, v46
	v_min_u32_e32 v40, v40, v46
	v_max_u32_e32 v46, v44, v43
	v_min_u32_e32 v43, v44, v43
	v_max_u32_e32 v44, v45, v49
	v_min_u32_e32 v45, v45, v49
	v_max_u32_e32 v49, v41, v37
	v_min_u32_e32 v37, v41, v37
	v_max_u32_e32 v41, v47, v42
	v_min_u32_e32 v42, v47, v42
	v_max_u32_e32 v47, v48, v35
	v_min_u32_e32 v35, v48, v35
	v_max_u32_e32 v48, v50, v39
	v_min_u32_e32 v39, v50, v39
	v_max_u32_e32 v50, v36, v34
	v_min_u32_e32 v34, v36, v34
	v_max_u32_e32 v36, v38, v41
	v_min_u32_e32 v38, v38, v41
	v_max_u32_e32 v41, v46, v47
	v_min_u32_e32 v46, v46, v47
	v_max_u32_e32 v47, v44, v48
	v_min_u32_e32 v44, v44, v48
	v_max_u32_e32 v48, v49, v50
	v_min_u32_e32 v49, v49, v50
	v_max_u32_e32 v50, v40, v42
	v_min_u32_e32 v40, v40, v42
	v_max_u32_e32 v42, v43, v35
	v_min_u32_e32 v35, v43, v35
	v_max_u32_e32 v43, v45, v39
	v_min_u32_e32 v39, v45, v39
	v_max_u32_e32 v45, v37, v34
	v_min_u32_e32 v34, v37, v34
	v_max_u32_e32 v37, v36, v47
	v_min_u32_e32 v47, v36, v47
	v_max_u32_e32 v51, v41, v48
	v_min_u32_e32 v41, v41, v48
	v_max_u32_e32 v48, v38, v44
	v_min_u32_e32 v44, v38, v44
	v_max_u32_e32 v52, v46, v49
	v_min_u32_e32 v46, v46, v49
	v_max_u32_e32 v49, v50, v43
	v_min_u32_e32 v50, v50, v43
	v_max_u32_e32 v53, v42, v45
	v_min_u32_e32 v55, v42, v45
	v_max_u32_e32 v58, v40, v39
	v_min_u32_e32 v59, v40, v39
	v_max_u32_e32 v60, v35, v34
	v_min_u32_e32 v34, v35, v34
	v_max_u32_e32 v36, v37, v51
	v_min_u32_e32 v37, v37, v51
	v_max_u32_e32 v38, v47, v41
	v_min_u32_e32 v39, v47, v41
	v_max_u32_e32 v40, v48, v52
	v_min_u32_e32 v41, v48, v52
	v_max_u32_e32 v42, v44, v46
	v_min_u32_e32 v43, v44, v46
	v_max_u32_e32 v44, v49, v53
	v_min_u32_e32 v45, v49, v53
	v_max_u32_e32 v54, v50, v55
	v_min_u32_e32 v56, v50, v55
	v_max_u32_e32 v57, v58, v60
	v_min_u32_e32 v66, v58, v60
	v_max_u32_e32 v67, v59, v34
	v_min_u32_e32 v68, v59, v34
	v_mov_b32_e32 v69, v36
	v_mov_b32_e32 v158, v37
	v_mov_b32_e32 v159, v38
	v_mov_b32_e32 v160, v39
	v_mov_b32_e32 v161, v40
	v_mov_b32_e32 v162, v41
	v_mov_b32_e32 v163, v42
	v_mov_b32_e32 v97, v43
	v_mov_b32_e32 v53, v44
	v_mov_b32_e32 v52, v45
	v_mov_b32_e32 v51, v54
	v_mov_b32_e32 v50, v56
	v_mov_b32_e32 v49, v57
	v_mov_b32_e32 v48, v66
	v_mov_b32_e32 v47, v67
	v_mov_b32_e32 v46, v68
	v_permlane32_swap_b32_e32 v36, v69
	v_permlane32_swap_b32_e32 v37, v158
	v_permlane32_swap_b32_e32 v38, v159
	v_permlane32_swap_b32_e32 v39, v160
	v_permlane32_swap_b32_e32 v40, v161
	v_permlane32_swap_b32_e32 v41, v162
	v_permlane32_swap_b32_e32 v42, v163
	v_permlane32_swap_b32_e32 v43, v97
	v_permlane32_swap_b32_e32 v44, v53
	v_permlane32_swap_b32_e32 v45, v52
	v_permlane32_swap_b32_e32 v54, v51
	v_permlane32_swap_b32_e32 v56, v50
	v_permlane32_swap_b32_e32 v57, v49
	v_permlane32_swap_b32_e32 v66, v48
	v_permlane32_swap_b32_e32 v67, v47
	v_permlane32_swap_b32_e32 v68, v46
	v_max_u32_e32 v59, v70, v157
	v_max_u32_e32 v60, v71, v156
	v_max_u32_e32 v61, v72, v155
	v_max_u32_e32 v62, v73, v154
	v_max_u32_e32 v63, v74, v153
	v_max_u32_e32 v64, v75, v152
	v_max_u32_e32 v65, v76, v151
	v_max_u32_e32 v70, v77, v150
	v_max_u32_e32 v71, v134, v149
	v_max_u32_e32 v72, v135, v148
	v_max_u32_e32 v73, v136, v147
	v_max_u32_e32 v74, v137, v146
	v_max_u32_e32 v75, v138, v145
	v_max_u32_e32 v76, v139, v144
	v_max_u32_e32 v77, v140, v143
	v_max_u32_e32 v96, v141, v142
	v_max_u32_e32 v55, v59, v71
	v_max_u32_e32 v135, v60, v72
	v_max_u32_e32 v136, v61, v73
	v_max_u32_e32 v137, v62, v74
	v_max_u32_e32 v138, v63, v75
	v_max_u32_e32 v139, v64, v76
	v_max_u32_e32 v140, v65, v77
	v_max_u32_e32 v141, v70, v96
	v_max_u32_e32 v46, v36, v46
	v_max_u32_e32 v47, v37, v47
	v_max_u32_e32 v48, v38, v48
	v_max_u32_e32 v49, v39, v49
	v_max_u32_e32 v50, v40, v50
	v_max_u32_e32 v51, v41, v51
	v_max_u32_e32 v52, v42, v52
	v_max_u32_e32 v53, v43, v53
	v_max_u32_e32 v97, v44, v97
	v_max_u32_e32 v134, v45, v163
	v_max_u32_e32 v143, v54, v162
	v_max_u32_e32 v149, v56, v161
	v_max_u32_e32 v150, v57, v160
	v_max_u32_e32 v151, v66, v159
	v_max_u32_e32 v152, v67, v158
	v_max_u32_e32 v153, v68, v69
	v_max_u32_e32 v216, v59, v71
	v_min_u32_e32 v224, v59, v71
	v_max_u32_e32 v217, v60, v72
	v_min_u32_e32 v225, v60, v72
	v_max_u32_e32 v218, v61, v73
	v_min_u32_e32 v226, v61, v73
	v_max_u32_e32 v219, v62, v74
	v_min_u32_e32 v227, v62, v74
	v_max_u32_e32 v220, v63, v75
	v_min_u32_e32 v228, v63, v75
	v_max_u32_e32 v221, v64, v76
	v_min_u32_e32 v229, v64, v76
	v_max_u32_e32 v222, v65, v77
	v_min_u32_e32 v230, v65, v77
	v_max_u32_e32 v223, v70, v96
	v_min_u32_e32 v231, v70, v96
	v_max_u32_e32 v232, v216, v220
	v_min_u32_e32 v236, v216, v220
	v_max_u32_e32 v233, v217, v221
	v_min_u32_e32 v237, v217, v221
	v_max_u32_e32 v234, v218, v222
	v_min_u32_e32 v238, v218, v222
	v_max_u32_e32 v235, v219, v223
	v_min_u32_e32 v239, v219, v223
	v_max_u32_e32 v240, v224, v228
	v_min_u32_e32 v246, v224, v228
	v_max_u32_e32 v241, v225, v229
	v_min_u32_e32 v247, v225, v229
	v_max_u32_e32 v244, v226, v230
	v_min_u32_e32 v248, v226, v230
	v_max_u32_e32 v245, v227, v231
	v_min_u32_e32 v249, v227, v231
	v_max_u32_e32 v216, v232, v234
	v_min_u32_e32 v218, v232, v234
	v_max_u32_e32 v217, v233, v235
	v_min_u32_e32 v219, v233, v235
	v_max_u32_e32 v220, v236, v238
	v_min_u32_e32 v222, v236, v238
	v_max_u32_e32 v221, v237, v239
	v_min_u32_e32 v223, v237, v239
	v_max_u32_e32 v224, v240, v244
	v_min_u32_e32 v226, v240, v244
	v_max_u32_e32 v225, v241, v245
	v_min_u32_e32 v227, v241, v245
	v_max_u32_e32 v228, v246, v248
	v_min_u32_e32 v230, v246, v248
	v_max_u32_e32 v229, v247, v249
	v_min_u32_e32 v231, v247, v249
	v_max_u32_e32 v34, v216, v217
	v_min_u32_e32 v35, v216, v217
	v_max_u32_e32 v36, v218, v219
	v_min_u32_e32 v37, v218, v219
	v_max_u32_e32 v54, v220, v221
	v_min_u32_e32 v55, v220, v221
	v_max_u32_e32 v56, v222, v223
	v_min_u32_e32 v57, v222, v223
	v_max_u32_e32 v58, v224, v225
	v_min_u32_e32 v59, v224, v225
	v_max_u32_e32 v60, v226, v227
	v_min_u32_e32 v61, v226, v227
	v_max_u32_e32 v62, v228, v229
	v_min_u32_e32 v63, v228, v229
	v_max_u32_e32 v64, v230, v231
	v_min_u32_e32 v65, v230, v231
	v_max_u32_e32 v216, v46, v97
	v_min_u32_e32 v224, v46, v97
	v_max_u32_e32 v217, v47, v134
	v_min_u32_e32 v225, v47, v134
	v_max_u32_e32 v218, v48, v143
	v_min_u32_e32 v226, v48, v143
	v_max_u32_e32 v219, v49, v149
	v_min_u32_e32 v227, v49, v149
	v_max_u32_e32 v220, v50, v150
	v_min_u32_e32 v228, v50, v150
	v_max_u32_e32 v221, v51, v151
	v_min_u32_e32 v229, v51, v151
	v_max_u32_e32 v222, v52, v152
	v_min_u32_e32 v230, v52, v152
	v_max_u32_e32 v223, v53, v153
	v_min_u32_e32 v231, v53, v153
	v_max_u32_e32 v232, v216, v220
	v_min_u32_e32 v236, v216, v220
	v_max_u32_e32 v233, v217, v221
	v_min_u32_e32 v237, v217, v221
	v_max_u32_e32 v234, v218, v222
	v_min_u32_e32 v238, v218, v222
	v_max_u32_e32 v235, v219, v223
	v_min_u32_e32 v239, v219, v223
	v_max_u32_e32 v240, v224, v228
	v_min_u32_e32 v246, v224, v228
	v_max_u32_e32 v241, v225, v229
	v_min_u32_e32 v247, v225, v229
	v_max_u32_e32 v244, v226, v230
	v_min_u32_e32 v248, v226, v230
	v_max_u32_e32 v245, v227, v231
	v_min_u32_e32 v249, v227, v231
	v_max_u32_e32 v216, v232, v234
	v_min_u32_e32 v218, v232, v234
	v_max_u32_e32 v217, v233, v235
	v_min_u32_e32 v219, v233, v235
	v_max_u32_e32 v220, v236, v238
	v_min_u32_e32 v222, v236, v238
	v_max_u32_e32 v221, v237, v239
	v_min_u32_e32 v223, v237, v239
	v_max_u32_e32 v224, v240, v244
	v_min_u32_e32 v226, v240, v244
	v_max_u32_e32 v225, v241, v245
	v_min_u32_e32 v227, v241, v245
	v_max_u32_e32 v228, v246, v248
	v_min_u32_e32 v230, v246, v248
	v_max_u32_e32 v229, v247, v249
	v_min_u32_e32 v231, v247, v249
	v_max_u32_e32 v38, v216, v217
	v_min_u32_e32 v39, v216, v217
	v_max_u32_e32 v40, v218, v219
	v_min_u32_e32 v41, v218, v219
	v_max_u32_e32 v42, v220, v221
	v_min_u32_e32 v43, v220, v221
	v_max_u32_e32 v44, v222, v223
	v_min_u32_e32 v45, v222, v223
	v_max_u32_e32 v46, v224, v225
	v_min_u32_e32 v47, v224, v225
	v_max_u32_e32 v48, v226, v227
	v_min_u32_e32 v49, v226, v227
	v_max_u32_e32 v50, v228, v229
	v_min_u32_e32 v51, v228, v229
	v_max_u32_e32 v52, v230, v231
	v_min_u32_e32 v53, v230, v231
	v_ashrrev_i32_e32 v216, 31, v34
	v_ashrrev_i32_e32 v217, 31, v35
; __device__ __forceinline__ unsigned mono(float f) { const unsigned u = __float_as_uint(f); return (u & 0x80000000u) ? ~u : (u ^ 0x80000000u); }
; __device__ __forceinline__ float unmono(unsigned u) { return __uint_as_float((u & 0x80000000u) ? (u ^ 0x80000000u) : ~u); }
; __device__ __forceinline__ void topk_phase(LAS unsigned char* lds, const bf16_t* qp, const bf16_t* keys, const float* SU, const float* SV, int* sel_e, float* sel_g, float* sel_su, int G, int b) {
;     ...
;         float v1[16], v2[16];
; #pragma unroll
;         for (int i = 0; i < 16; ++i) { v1[i] = unmono(T[0][i] & ~127u); v2[i] = unmono(T[1][i] & ~127u); }
;         unsigned ck[16];
; #pragma unroll
;         for (int sidx = 0; sidx < 13; ++sidx) {
;             unsigned keyk[4];
; #pragma unroll
;             for (int k = 0; k < 4; ++k) {
;                 const int c = 4 * sidx + k;
;                 if (c < 50) { const int ci = cand_i(c), cj = cand_j(c); keyk[k] = (mono(v1[ci] + v2[cj]) & ~255u) | (unsigned)(255 - (ci * 16 + cj)); }
;                 else keyk[k] = 0u;
;             }
;             ck[sidx] = fq == 0 ? keyk[0] : fq == 1 ? keyk[1] : fq == 2 ? keyk[2] : keyk[3];
;         }
	v_ashrrev_i32_e32 v218, 31, v36
	v_ashrrev_i32_e32 v219, 31, v37
	v_ashrrev_i32_e32 v220, 31, v54
	v_ashrrev_i32_e32 v221, 31, v55
	v_ashrrev_i32_e32 v222, 31, v56
	v_ashrrev_i32_e32 v223, 31, v57
	v_ashrrev_i32_e32 v224, 31, v58
	v_ashrrev_i32_e32 v225, 31, v59
	v_ashrrev_i32_e32 v226, 31, v60
	v_ashrrev_i32_e32 v227, 31, v61
	v_ashrrev_i32_e32 v228, 31, v62
	v_ashrrev_i32_e32 v229, 31, v63
	v_ashrrev_i32_e32 v230, 31, v64
	v_ashrrev_i32_e32 v231, 31, v65
	v_bitop3_b32 v170, v34, v216, s12 bitop3:0x93
	v_bitop3_b32 v171, v35, v217, s12 bitop3:0x93
	v_bitop3_b32 v172, v36, v218, s12 bitop3:0x93
	v_bitop3_b32 v173, v37, v219, s12 bitop3:0x93
	v_bitop3_b32 v174, v54, v220, s12 bitop3:0x93
	v_bitop3_b32 v175, v55, v221, s12 bitop3:0x93
	v_bitop3_b32 v176, v56, v222, s12 bitop3:0x93
	v_bitop3_b32 v177, v57, v223, s12 bitop3:0x93
	v_bitop3_b32 v178, v58, v224, s12 bitop3:0x93
	v_bitop3_b32 v179, v59, v225, s12 bitop3:0x93
	v_bitop3_b32 v180, v60, v226, s12 bitop3:0x93
	v_bitop3_b32 v181, v61, v227, s12 bitop3:0x93
	v_bitop3_b32 v182, v62, v228, s12 bitop3:0x93
	v_bitop3_b32 v183, v63, v229, s12 bitop3:0x93
	v_bitop3_b32 v184, v64, v230, s12 bitop3:0x93
	v_bitop3_b32 v185, v65, v231, s12 bitop3:0x93
	v_ashrrev_i32_e32 v216, 31, v38
	v_ashrrev_i32_e32 v217, 31, v39
	v_ashrrev_i32_e32 v218, 31, v40
	v_ashrrev_i32_e32 v219, 31, v41
	v_ashrrev_i32_e32 v220, 31, v42
	v_ashrrev_i32_e32 v221, 31, v43
	v_ashrrev_i32_e32 v222, 31, v44
	v_ashrrev_i32_e32 v223, 31, v45
	v_ashrrev_i32_e32 v224, 31, v46
	v_ashrrev_i32_e32 v225, 31, v47
	v_ashrrev_i32_e32 v226, 31, v48
	v_ashrrev_i32_e32 v227, 31, v49
	v_ashrrev_i32_e32 v228, 31, v50
	v_ashrrev_i32_e32 v229, 31, v51
	v_ashrrev_i32_e32 v230, 31, v52
	v_ashrrev_i32_e32 v231, 31, v53
	v_bitop3_b32 v186, v38, v216, s12 bitop3:0x93
	v_bitop3_b32 v187, v39, v217, s12 bitop3:0x93
	v_bitop3_b32 v188, v40, v218, s12 bitop3:0x93
	v_bitop3_b32 v189, v41, v219, s12 bitop3:0x93
	v_bitop3_b32 v190, v42, v220, s12 bitop3:0x93
	v_bitop3_b32 v191, v43, v221, s12 bitop3:0x93
	v_bitop3_b32 v192, v44, v222, s12 bitop3:0x93
	v_bitop3_b32 v193, v45, v223, s12 bitop3:0x93
	v_bitop3_b32 v194, v46, v224, s12 bitop3:0x93
	v_bitop3_b32 v195, v47, v225, s12 bitop3:0x93
	v_bitop3_b32 v196, v48, v226, s12 bitop3:0x93
	v_bitop3_b32 v197, v49, v227, s12 bitop3:0x93
	v_bitop3_b32 v198, v50, v228, s12 bitop3:0x93
	v_bitop3_b32 v199, v51, v229, s12 bitop3:0x93
	v_bitop3_b32 v200, v52, v230, s12 bitop3:0x93
	v_bitop3_b32 v201, v53, v231, s12 bitop3:0x93
	v_cndmask_b32_e64 v250, v186, v187, s[16:17]
	v_cndmask_b32_e64 v250, v250, v188, s[18:19]
	v_cndmask_b32_e64 v250, v250, v189, s[20:21]
	v_cndmask_b32_e64 v251, v190, v191, s[16:17]
	v_cndmask_b32_e64 v251, v251, v192, s[18:19]
	v_cndmask_b32_e64 v251, v251, v193, s[20:21]
	v_cndmask_b32_e64 v252, v194, v195, s[16:17]
	v_cndmask_b32_e64 v252, v252, v196, s[18:19]
	v_cndmask_b32_e64 v252, v252, v197, s[20:21]
	v_cndmask_b32_e64 v253, v198, v199, s[16:17]
	v_cndmask_b32_e64 v253, v253, v200, s[18:19]
	v_cndmask_b32_e64 v253, v253, v201, s[20:21]
	v_add_f32_e32 v254, v170, v250
	v_ashrrev_i32_e32 v255, 31, v254
	v_bitop3_b32 v254, v254, v255, v132 bitop3:0x1e
	v_and_or_b32 v68, v254, s60, v203
	v_add_f32_e32 v254, v170, v251
	v_ashrrev_i32_e32 v255, 31, v254
	v_bitop3_b32 v254, v254, v255, v132 bitop3:0x1e
	v_and_or_b32 v69, v254, s60, v204
	v_add_f32_e32 v254, v170, v252
	v_ashrrev_i32_e32 v255, 31, v254
	v_bitop3_b32 v254, v254, v255, v132 bitop3:0x1e
	v_and_or_b32 v97, v254, s60, v205
	v_add_f32_e32 v254, v170, v253
	v_ashrrev_i32_e32 v255, 31, v254
	v_bitop3_b32 v254, v254, v255, v132 bitop3:0x1e
	v_and_or_b32 v134, v254, s60, v206
	v_add_f32_e32 v254, v171, v250
	v_ashrrev_i32_e32 v255, 31, v254
	v_bitop3_b32 v254, v254, v255, v132 bitop3:0x1e
	v_and_or_b32 v142, v254, s60, v207
	v_add_f32_e32 v254, v171, v251
	v_ashrrev_i32_e32 v255, 31, v254
	v_bitop3_b32 v254, v254, v255, v132 bitop3:0x1e
	v_and_or_b32 v143, v254, s60, v208
	v_add_f32_e32 v254, v172, v250
	v_ashrrev_i32_e32 v255, 31, v254
	v_bitop3_b32 v254, v254, v255, v132 bitop3:0x1e
	v_and_or_b32 v144, v254, s60, v209
	v_cndmask_b32_e64 v232, v172, v173, s[16:17]
	v_cndmask_b32_e64 v232, v232, v173, s[22:23]
	v_cndmask_b32_e64 v233, v190, v186, s[16:17]
	v_cndmask_b32_e64 v233, v233, v187, s[18:19]
	v_cndmask_b32_e64 v233, v233, v188, s[20:21]
	v_add_f32_e32 v254, v232, v233
	v_ashrrev_i32_e32 v255, 31, v254
	v_bitop3_b32 v254, v254, v255, v132 bitop3:0x1e
	v_and_or_b32 v145, v254, s60, v210
	v_cndmask_b32_e64 v234, v173, v174, s[16:17]
	v_cndmask_b32_e64 v234, v234, v174, s[22:23]
	v_cndmask_b32_e64 v235, v189, v186, s[16:17]
	v_cndmask_b32_e64 v235, v235, v187, s[18:19]
	v_cndmask_b32_e64 v235, v235, v188, s[20:21]
	v_add_f32_e32 v254, v234, v235
	v_ashrrev_i32_e32 v255, 31, v254
	v_bitop3_b32 v254, v254, v255, v132 bitop3:0x1e
	v_and_or_b32 v135, v254, s60, v211
	v_cndmask_b32_e64 v236, v175, v176, s[22:23]
	v_cndmask_b32_e64 v237, v186, v187, s[24:25]
	v_add_f32_e32 v254, v236, v237
	v_ashrrev_i32_e32 v255, 31, v254
	v_bitop3_b32 v254, v254, v255, v132 bitop3:0x1e
	v_and_or_b32 v136, v254, s60, v212
	v_cndmask_b32_e64 v238, v177, v178, s[18:19]
	v_cndmask_b32_e64 v238, v238, v179, s[20:21]
	v_cndmask_b32_e64 v239, v186, v187, s[16:17]
	v_add_f32_e32 v254, v238, v239
	v_ashrrev_i32_e32 v255, 31, v254
	v_bitop3_b32 v254, v254, v255, v132 bitop3:0x1e
	v_and_or_b32 v70, v254, s60, v213
	v_cndmask_b32_e64 v240, v180, v181, s[16:17]
	v_cndmask_b32_e64 v240, v240, v182, s[18:19]
	v_cndmask_b32_e64 v240, v240, v183, s[20:21]
	v_add_f32_e32 v254, v240, v186
	v_ashrrev_i32_e32 v255, 31, v254
	v_bitop3_b32 v254, v254, v255, v132 bitop3:0x1e
; __device__ __forceinline__ unsigned mono(float f) { const unsigned u = __float_as_uint(f); return (u & 0x80000000u) ? ~u : (u ^ 0x80000000u); }
; __device__ __forceinline__ void topk_phase(LAS unsigned char* lds, const bf16_t* qp, const bf16_t* keys, const float* SU, const float* SV, int* sel_e, float* sel_g, float* sel_su, int G, int b) {
;     ...
;                 if (c < 50) { const int ci = cand_i(c), cj = cand_j(c); keyk[k] = (mono(v1[ci] + v2[cj]) & ~255u) | (unsigned)(255 - (ci * 16 + cj)); }
;                 else keyk[k] = 0u;
;             }
;             ck[sidx] = fq == 0 ? keyk[0] : fq == 1 ? keyk[1] : fq == 2 ? keyk[2] : keyk[3];
;         }
;         ck[13] = 0u; ck[14] = 0u; ck[15] = 0u;
;         SN_SORT16(ck);
;         TOPK_XMERGE(ck, 16); TOPK_XMERGE(ck, 32);
	v_and_or_b32 v71, v254, s60, v214
	v_cndmask_b32_e64 v241, v184, v185, s[16:17]
	v_add_f32_e32 v254, v241, v186
	v_ashrrev_i32_e32 v255, 31, v254
	v_bitop3_b32 v254, v254, v255, v132 bitop3:0x1e
	v_and_or_b32 v67, v254, s60, v215
	v_cndmask_b32_e64 v67, v67, 0, s[22:23]
	v_max_u32_e32 v66, v68, v69
	v_min_u32_e32 v68, v68, v69
	v_max_u32_e32 v69, v97, v134
	v_min_u32_e32 v72, v97, v134
	v_max_u32_e32 v73, v66, v69
	v_min_u32_e32 v66, v66, v69
	v_max_u32_e32 v69, v68, v72
	v_min_u32_e32 v68, v68, v72
	v_max_u32_e32 v72, v69, v66
	v_min_u32_e32 v66, v69, v66
	v_max_u32_e32 v69, v142, v143
	v_min_u32_e32 v74, v142, v143
	v_max_u32_e32 v75, v144, v145
	v_min_u32_e32 v76, v144, v145
	v_max_u32_e32 v77, v69, v75
	v_min_u32_e32 v69, v69, v75
	v_max_u32_e32 v75, v74, v76
	v_min_u32_e32 v74, v74, v76
	v_max_u32_e32 v76, v75, v69
	v_min_u32_e32 v69, v75, v69
	v_max_u32_e32 v75, v73, v77
	v_min_u32_e32 v73, v73, v77
	v_max_u32_e32 v77, v66, v69
	v_min_u32_e32 v66, v66, v69
	v_max_u32_e32 v69, v77, v73
	v_min_u32_e32 v73, v77, v73
	v_max_u32_e32 v77, v72, v76
	v_min_u32_e32 v72, v72, v76
	v_max_u32_e32 v76, v68, v74
	v_min_u32_e32 v68, v68, v74
	v_max_u32_e32 v74, v76, v72
	v_min_u32_e32 v72, v76, v72
	v_max_u32_e32 v76, v77, v69
	v_min_u32_e32 v69, v77, v69
	v_max_u32_e32 v77, v74, v73
	v_min_u32_e32 v73, v74, v73
	v_max_u32_e32 v74, v72, v66
	v_min_u32_e32 v66, v72, v66
	v_max_u32_e32 v72, v135, v136
	v_min_u32_e32 v96, v135, v136
	v_max_u32_e32 v97, v70, v71
	v_min_u32_e32 v70, v70, v71
	v_max_u32_e32 v71, v72, v97
	v_min_u32_e32 v72, v72, v97
	v_max_u32_e32 v97, v96, v70
	v_min_u32_e32 v134, v97, v72
	v_max_u32_e32 v135, v71, v67
	v_min_u32_e32 v67, v71, v67
	v_min_u32_e32 v70, v96, v70
	v_max_u32_e32 v71, v134, v67
	v_min_u32_e32 v134, v134, v67
	v_max_u32_e32 v96, v97, v72
	v_med3_u32 v67, v97, v72, v67
	v_max_u32_e32 v72, v70, v134
	v_min_u32_e32 v70, v70, v134
	v_max_u32_e32 v71, v96, v71
	v_max_u32_e32 v96, v75, v135
	v_min_u32_e32 v75, v75, v135
	v_max_u32_e32 v97, v73, v70
	v_min_u32_e32 v70, v73, v70
	v_max_u32_e32 v73, v97, v75
	v_min_u32_e32 v75, v97, v75
	v_max_u32_e32 v97, v69, v67
	v_min_u32_e32 v67, v69, v67
	v_max_u32_e32 v69, v66, v67
	v_min_u32_e32 v66, v66, v67
	v_max_u32_e32 v67, v97, v73
	v_min_u32_e32 v73, v97, v73
	v_max_u32_e32 v97, v69, v75
	v_min_u32_e32 v69, v69, v75
	v_max_u32_e32 v75, v66, v70
	v_min_u32_e32 v66, v66, v70
	v_max_u32_e32 v70, v76, v71
	v_min_u32_e32 v71, v76, v71
	v_max_u32_e32 v76, v74, v71
	v_min_u32_e32 v71, v74, v71
	v_max_u32_e32 v74, v77, v72
	v_min_u32_e32 v72, v77, v72
	v_max_u32_e32 v77, v68, v72
	v_min_u32_e32 v68, v68, v72
	v_max_u32_e32 v72, v74, v76
	v_min_u32_e32 v74, v74, v76
	v_max_u32_e32 v76, v77, v71
	v_min_u32_e32 v71, v77, v71
	v_max_u32_e32 v77, v70, v67
	v_min_u32_e32 v67, v70, v67
	v_max_u32_e32 v70, v72, v73
	v_min_u32_e32 v72, v72, v73
	v_max_u32_e32 v73, v74, v97
	v_min_u32_e32 v74, v74, v97
	v_max_u32_e32 v97, v76, v69
	v_min_u32_e32 v69, v76, v69
	v_max_u32_e32 v76, v71, v75
	v_min_u32_e32 v71, v71, v75
	v_max_u32_e32 v75, v68, v66
	v_min_u32_e32 v66, v68, v66
	v_mov_b32_e32 v68, v96
	v_mov_b32_e32 v134, v77
	v_mov_b32_e32 v135, v67
	v_mov_b32_e32 v136, v70
	v_mov_b32_e32 v137, v72
	v_mov_b32_e32 v138, v73
	v_mov_b32_e32 v139, v74
	v_mov_b32_e32 v140, v97
	v_mov_b32_e32 v141, v69
	v_mov_b32_e32 v142, v76
	v_mov_b32_e32 v143, v71
	v_mov_b32_e32 v144, v75
	v_mov_b32_e32 v145, v66
	v_mov_b32_e32 v146, 0
	v_mov_b32_e32 v147, 0
	v_permlane16_swap_b32_e32 v96, v68
	v_permlane16_swap_b32_e32 v77, v134
	v_permlane16_swap_b32_e32 v67, v135
	v_permlane16_swap_b32_e32 v70, v136
	v_permlane16_swap_b32_e32 v72, v137
	v_permlane16_swap_b32_e32 v73, v138
	v_permlane16_swap_b32_e32 v74, v139
	v_permlane16_swap_b32_e32 v97, v140
	v_permlane16_swap_b32_e32 v69, v141
	v_permlane16_swap_b32_e32 v76, v142
	v_permlane16_swap_b32_e32 v71, v143
; __device__ __forceinline__ void topk_phase(LAS unsigned char* lds, const bf16_t* qp, const bf16_t* keys, const float* SU, const float* SV, int* sel_e, float* sel_g, float* sel_su, int G, int b) {
;     ...
;         TOPK_XMERGE(ck, 16); TOPK_XMERGE(ck, 32);
;         if (fq == 0) {
; #pragma unroll
;             for (int i = 0; i < 16; ++i) { wl[i] = T[0][i]; wl[16 + i] = T[1][i]; }
;         }
	v_permlane16_swap_b32_e32 v75, v144
	v_permlane16_swap_b32_e32 v66, v145
	v_permlane16_swap_b32_e32 v146, v147
	v_max_u32_e32 v96, v96, v147
	v_max_u32_e32 v77, v77, v147
	v_max_u32_e32 v67, v67, v147
	v_max_u32_e32 v70, v70, v145
	v_max_u32_e32 v72, v72, v144
	v_max_u32_e32 v73, v73, v143
	v_max_u32_e32 v74, v74, v142
	v_max_u32_e32 v97, v97, v141
	v_max_u32_e32 v69, v69, v140
	v_max_u32_e32 v76, v76, v139
	v_max_u32_e32 v71, v71, v138
	v_max_u32_e32 v75, v75, v137
	v_max_u32_e32 v66, v66, v136
	v_max_u32_e32 v135, v146, v135
	v_max_u32_e32 v134, v146, v134
	v_max_u32_e32 v68, v146, v68
	v_max_u32_e32 v136, v96, v69
	v_min_u32_e32 v69, v96, v69
	v_max_u32_e32 v96, v77, v76
	v_min_u32_e32 v76, v77, v76
	v_max_u32_e32 v77, v67, v71
	v_min_u32_e32 v67, v67, v71
	v_max_u32_e32 v71, v70, v75
	v_min_u32_e32 v70, v70, v75
	v_max_u32_e32 v75, v72, v66
	v_min_u32_e32 v66, v72, v66
	v_max_u32_e32 v72, v73, v135
	v_min_u32_e32 v73, v73, v135
	v_max_u32_e32 v135, v74, v134
	v_min_u32_e32 v74, v74, v134
	v_max_u32_e32 v134, v97, v68
	v_min_u32_e32 v68, v97, v68
	v_max_u32_e32 v97, v136, v75
	v_min_u32_e32 v75, v136, v75
	v_max_u32_e32 v136, v96, v72
	v_min_u32_e32 v72, v96, v72
	v_max_u32_e32 v96, v77, v135
	v_min_u32_e32 v77, v77, v135
	v_max_u32_e32 v135, v71, v134
	v_min_u32_e32 v71, v71, v134
	v_max_u32_e32 v134, v69, v66
	v_min_u32_e32 v66, v69, v66
	v_max_u32_e32 v69, v76, v73
	v_min_u32_e32 v73, v76, v73
	v_max_u32_e32 v76, v67, v74
	v_min_u32_e32 v67, v67, v74
	v_max_u32_e32 v74, v70, v68
	v_min_u32_e32 v68, v70, v68
	v_max_u32_e32 v70, v97, v96
	v_min_u32_e32 v96, v97, v96
	v_max_u32_e32 v97, v136, v135
	v_min_u32_e32 v135, v136, v135
	v_max_u32_e32 v136, v75, v77
	v_min_u32_e32 v75, v75, v77
	v_max_u32_e32 v77, v72, v71
	v_min_u32_e32 v137, v72, v71
	v_max_u32_e32 v138, v134, v76
	v_min_u32_e32 v134, v134, v76
	v_max_u32_e32 v76, v69, v74
	v_min_u32_e32 v139, v69, v74
	v_max_u32_e32 v140, v66, v67
	v_min_u32_e32 v141, v66, v67
	v_max_u32_e32 v142, v73, v68
	v_min_u32_e32 v143, v73, v68
	v_max_u32_e32 v66, v70, v97
	v_min_u32_e32 v67, v70, v97
	v_max_u32_e32 v68, v96, v135
	v_min_u32_e32 v69, v96, v135
	v_max_u32_e32 v70, v136, v77
	v_min_u32_e32 v71, v136, v77
	v_max_u32_e32 v72, v75, v137
	v_min_u32_e32 v73, v75, v137
	v_max_u32_e32 v74, v138, v76
	v_min_u32_e32 v75, v138, v76
	v_max_u32_e32 v76, v134, v139
	v_min_u32_e32 v77, v134, v139
	v_max_u32_e32 v96, v140, v142
	v_min_u32_e32 v97, v140, v142
	v_max_u32_e32 v134, v141, v143
	v_min_u32_e32 v135, v141, v143
	v_mov_b32_e32 v136, v66
	v_mov_b32_e32 v137, v67
	v_mov_b32_e32 v138, v68
	v_mov_b32_e32 v139, v69
	v_mov_b32_e32 v140, v70
	v_mov_b32_e32 v141, v71
	v_mov_b32_e32 v142, v72
	v_mov_b32_e32 v143, v73
	v_mov_b32_e32 v144, v74
	v_mov_b32_e32 v145, v75
	v_mov_b32_e32 v146, v76
	v_mov_b32_e32 v147, v77
	v_mov_b32_e32 v148, v96
	v_mov_b32_e32 v149, v97
	v_mov_b32_e32 v150, v134
	v_mov_b32_e32 v151, v135
	v_permlane32_swap_b32_e32 v66, v136
	v_permlane32_swap_b32_e32 v67, v137
	v_permlane32_swap_b32_e32 v68, v138
	v_permlane32_swap_b32_e32 v69, v139
	v_permlane32_swap_b32_e32 v70, v140
	v_permlane32_swap_b32_e32 v71, v141
	v_permlane32_swap_b32_e32 v72, v142
	v_permlane32_swap_b32_e32 v73, v143
	v_permlane32_swap_b32_e32 v74, v144
	v_permlane32_swap_b32_e32 v75, v145
	v_permlane32_swap_b32_e32 v76, v146
	v_permlane32_swap_b32_e32 v77, v147
	v_permlane32_swap_b32_e32 v96, v148
	v_permlane32_swap_b32_e32 v97, v149
	v_permlane32_swap_b32_e32 v134, v150
	v_permlane32_swap_b32_e32 v135, v151
	s_and_saveexec_b64 s[0:1], s[40:41]
	s_cbranch_execz .LBB0_739
	ds_write_b128 v83, v[34:37]
	ds_write_b128 v83, v[38:41] offset:64
	ds_write_b128 v83, v[54:57] offset:16
	ds_write_b128 v83, v[42:45] offset:80
	ds_write_b128 v83, v[58:61] offset:32
	ds_write_b128 v83, v[46:49] offset:96
	ds_write_b128 v83, v[62:65] offset:48
	ds_write_b128 v83, v[50:53] offset:112
